# P7,P8: the lagging half-workgroup's stagger barrier moved behind its next() so next() no longer runs beside the leading half's first MFMA segment
# baseline (speedup 1.0000x reference)
; #define PG8_STAGE(bufoff, gbase, voff) do { if constexpr (!(Sched::CRIP & 2)) _Pragma("unroll") for (int _i = 0; _i < 2; ++_i) { unsigned _o = (voff)[_i]; asm volatile("" : "+v"(_o)); \
;         __builtin_amdgcn_global_load_lds((const unsigned*)((const char*)(gbase) + _o), (LAS unsigned*)(lds + (bufoff) + ldsw + _i * 8192), 16, 0, 0); } } while (0)
; #define PG8_WAIT_V(n) asm volatile("s_waitcnt vmcnt(" #n ")" ::: "memory")
; #define PG8_BAR __builtin_amdgcn_s_barrier()
; template <class Epi, class Sched>
; __device__ __forceinline__ void gemm_phase(LAS unsigned char* lds, const Sched& S, const Epi& E) {
;     ...
;     PG8_STAGE(PG8_SB(0, 0), cB + PG8_KT(crot, 0), voffB); PG8_STAGE(PG8_SB(0, 1), cB + hstep + PG8_KT(crot, 0), voffB); PG8_STAGE(PG8_SA(0, 0), cA + PG8_KT(crot, 0), vA[0]); PG8_STAGE(PG8_SA(0, 1), cA + PG8_KT(crot, 0), vA[1]);
;     if (wr == 1) PG8_BAR;
;     PG8_WAIT_V(2); PG8_BAR;
;     PG8_STAGE(PG8_SB(1, 0), cB + PG8_KT(crot, 1), voffB); PG8_STAGE(PG8_SA(1, 0), cA + PG8_KT(crot, 1), vA[0]); PG8_STAGE(PG8_SB(1, 1), cB + hstep + PG8_KT(crot, 1), voffB);
;     PG8_WAIT_V(6); PG8_BAR;
;     ...
;                 for (int i = 0; i < 2; ++i) { int R, C; stage_rc(tz * 16 + i * 8192, R, C);
; #pragma unroll
;                     for (int h = 0; h < 2; ++h) vA[h][i] = (unsigned)(lidx[h * HALF + R] * RP + C * 2); } } }
.LBB0_724:
	s_add_u32 s12, s88, 0x3a800000
	s_addc_u32 s13, s89, 0
	s_lshl_b32 s2, s2, 12
	s_addk_i32 s7, 0x80
	s_lshl_b32 s14, s3, 13
	s_and_b32 s15, s2, 0x3000
	s_and_b32 s7, s7, 0x780
	s_add_u32 s2, s28, s7
	v_mov_b32_e32 v2, v1
	s_waitcnt vmcnt(2)
	s_barrier
	s_addc_u32 s3, s29, 0
	s_add_i32 m0, s39, 0x18000
	v_lshlrev_b32_e32 v3, 6, v0
	global_load_lds_dwordx4 v2, s[2:3]
	v_mov_b32_e32 v2, v190
	s_add_i32 m0, s39, 0x1a000
	v_lshlrev_b32_e32 v5, 2, v0
	global_load_lds_dwordx4 v2, s[2:3]
	s_add_u32 s2, s58, s7
	s_addc_u32 s3, s59, 0
	v_mov_b32_e32 v2, v192
	s_add_i32 s70, s39, 0x8000
	s_mov_b32 m0, s70
	s_add_i32 s71, s39, 0xa000
	global_load_lds_dwordx4 v2, s[2:3]
	v_mov_b32_e32 v2, v194
	s_mov_b32 m0, s71
	v_and_b32_e32 v3, 0x3c0, v3
	global_load_lds_dwordx4 v2, s[2:3]
	s_add_u32 s2, s4, s7
	v_mov_b32_e32 v2, v1
	s_addc_u32 s3, s5, 0
	s_add_i32 m0, s39, 0x1c000
	v_and_b32_e32 v6, 32, v5
	global_load_lds_dwordx4 v2, s[2:3]
	v_mov_b32_e32 v2, v190
	s_add_i32 m0, s39, 0x1e000
	s_cmpk_lt_u32 s6, 0x100
	global_load_lds_dwordx4 v2, s[2:3]
	v_and_b32_e32 v2, 48, v0
	v_or_b32_e32 v4, v3, v2
	v_bitop3_b32 v2, v3, v6, v2 bitop3:0x36
	v_bitop3_b32 v3, s14, v4, v6 bitop3:0xf6
	v_or_b32_e32 v196, s15, v2
	s_cselect_b64 s[14:15], -1, 0
	s_add_i32 s3, 0, 0x27d04
	v_writelane_b32 v255, s3, 55
	s_add_i32 s3, 0, 0x27d4c
	v_writelane_b32 v255, s3, 56
	s_add_i32 s3, 0, 0x27d54
	v_writelane_b32 v255, s3, 57
	s_add_i32 s3, 0, 0x27d5c
	v_writelane_b32 v255, s3, 58
	s_add_i32 s3, 0, 0x27d64
	s_waitcnt vmcnt(0)
	v_writelane_b32 v255, s3, 59
	s_add_i32 s3, 0, 0x27d6c
	s_mov_b32 s4, 0
	s_add_i32 s2, 0, 0x27d80
	v_writelane_b32 v255, s3, 60
	s_add_i32 s3, 0, 0x27d74
	v_mov_b32_e32 v187, 0
	v_add_u32_e32 v197, s60, v5
	s_ashr_i32 s96, s96, 31
	s_add_i32 s9, 0, 0x27d0c
	s_add_i32 s8, 0, 0x27d14
	s_add_i32 s17, 0, 0x27d1c
	s_add_i32 s50, 0, 0x27d24
	s_add_i32 s10, 0, 0x27d2c
	s_add_i32 s11, 0, 0x27d34
	s_add_i32 s56, 0, 0x27d3c
	s_add_i32 s57, 0, 0x27d44
	v_writelane_b32 v255, s3, 61
	s_add_i32 s91, 0, 0x27d7c
	v_lshlrev_b32_e32 v198, 2, v0
	s_add_i32 s92, 0, 0x10000
	s_add_i32 s93, 0, 0x14000
	s_mov_b32 s5, s4
	s_mov_b32 s6, s4
	s_mov_b32 s7, s4
	s_mov_b32 s16, 0xc01d265f
	s_mov_b32 s94, 0xc0e00000
	v_mov_b32_e32 v199, s2
	v_add_u32_e32 v200, 0, v3
	v_mov_b32_e32 v201, 1
	v_mov_b32_e32 v42, 0xba1d265f
	v_mov_b32_e32 v46, 0x39800000
	v_mov_b32_e32 v202, 0x40e00000
	v_mov_b32_e32 v188, 0x3fd083aa
	s_mov_b32 s95, s4
	s_mov_b64 s[24:25], s[28:29]
	s_barrier
	v_mov_b32_e32 v4, v0
	s_nop 0
	v_ashrrev_i32_e32 v6, 31, v4
	v_lshrrev_b32_e32 v6, 26, v6
	v_lshlrev_b32_e32 v5, 4, v4
	v_add_u32_e32 v6, v4, v6
	v_bfe_i32 v4, v4, 27, 1
	v_lshrrev_b32_e32 v4, 22, v4
	v_add_u32_e32 v4, v5, v4
	v_and_b32_e32 v4, 0xfffffc00, v4
	v_sub_u32_e32 v4, v5, v4
	v_lshrrev_b32_e32 v7, 4, v4
	v_bitop3_b32 v4, v7, v4, 32 bitop3:0x6c
	v_ashrrev_i32_e32 v7, 31, v4
	v_lshrrev_b32_e32 v7, 26, v7
	v_ashrrev_i32_e32 v6, 6, v6
	v_add_u32_e32 v7, v4, v7
	v_ashrrev_i32_e32 v8, 6, v7
	v_lshlrev_b32_e32 v6, 5, v6
	v_and_b32_e32 v9, 32, v6
	v_and_b32_e32 v10, 0xc0, v7
	v_lshlrev_b32_e32 v7, 2, v8
	v_and_b32_e32 v6, 0xffffffc0, v6
	v_add3_u32 v6, s60, v7, v6
	v_mov_b32_e32 v246, v6
	v_sub_u32_e32 v4, v4, v10
	v_ashrrev_i16_sdwa v4, v201, sext(v4) dst_sel:DWORD dst_unused:UNUSED_PAD src0_sel:DWORD src1_sel:BYTE_0
	v_bfe_i32 v4, v4, 0, 16
	v_add_lshl_u32 v4, v9, v4, 1
	v_mov_b32_e32 v247, v4
	v_add_u32_e32 v4, 0x2000, v5
	v_ashrrev_i32_e32 v5, 31, v4
	v_lshrrev_b32_e32 v5, 22, v5
	v_add_u32_e32 v5, v4, v5
	v_ashrrev_i32_e32 v5, 10, v5
	v_mul_i32_i24_e32 v6, 0x400, v5
	v_sub_u32_e32 v4, v4, v6
	v_lshrrev_b32_e32 v6, 4, v4
	v_bitop3_b32 v4, v6, v4, 32 bitop3:0x6c
	v_ashrrev_i32_e32 v6, 31, v4
	v_lshrrev_b32_e32 v6, 26, v6
	v_add_u32_e32 v6, v4, v6
	v_ashrrev_i32_e32 v7, 6, v6
	v_lshlrev_b32_e32 v5, 5, v5
	v_and_b32_e32 v8, 32, v5
	v_and_b32_e32 v9, 0xc0, v6
	v_lshlrev_b32_e32 v6, 2, v7
	v_and_b32_e32 v5, 0xffffffc0, v5
	v_add3_u32 v5, s60, v6, v5
	v_mov_b32_e32 v248, v5
	v_sub_u32_e32 v4, v4, v9
	v_ashrrev_i16_sdwa v4, v201, sext(v4) dst_sel:DWORD dst_unused:UNUSED_PAD src0_sel:DWORD src1_sel:BYTE_0
	v_bfe_i32 v4, v4, 0, 16
	v_add_lshl_u32 v4, v8, v4, 1
	v_mov_b32_e32 v249, v4
	s_mov_b32 s100, 0
	s_branch .LBB0_727

; #define PG8_BAR __builtin_amdgcn_s_barrier()
; template <class Epi, class Sched>
; __device__ __forceinline__ void gemm_phase(LAS unsigned char* lds, const Sched& S, const Epi& E) {
;     ...
;         const bool has_next = S.next(ui + 1, nxt);
;         const char* nA = has_next ? nxt.aBase : cA; const char* nB = has_next ? nxt.bBase : cB;
;         const int nrot = has_next ? KROT(nxt.pm, nxt.pn) : crot;
;     ...
;         if (wr == 1) PG8_BAR;
.LBB0_729:
	s_cmp_lg_u32 s100, 0
	s_cbranch_scc0 .Lstag7
	s_barrier

; __device__ __forceinline__ unsigned pk4_fp8(float a, float b, float c, float d) { int v = 0; v = __builtin_amdgcn_cvt_pk_fp8_f32(a, b, v, false); v = __builtin_amdgcn_cvt_pk_fp8_f32(c, d, v, true); return (unsigned)v; }
;     __device__ __forceinline__ void operator()(const f32x4 (&acc)[2][2][4][2], const pg8::Unit& u, const Pre& q, int wr, int wc, int fr, int fq) const {
;         const int row0 = u.pm * 256 + wr * 64 + fr, f0w = u.pn * 128 + wc * 32;
;         constexpr float DS = 1.0f / (FP8_SA * FP8_SW);
;         f32x4 dsk = (f32x4){DS * KP, DS * KP, DS * KP, DS * KP}, dsu = (f32x4){DS, DS, DS, DS}; asm volatile("" : "+v"(dsk), "+v"(dsu));
; #pragma unroll
;         for (int ai = 0; ai < 2; ++ai)
; #pragma unroll
;             for (int mp = 0; mp < 2; ++mp) { unsigned lo[2], hi[2];
; #pragma unroll
;                 for (int mm = 0; mm < 2; ++mm) { const int m = 2 * mp + mm; float h[8];
; #pragma unroll
;                     for (int n = 0; n < 2; ++n) { const f32x4 gk = __builtin_elementwise_fma(acc[ai][0][m][n], dsk, q.bg[n]), up = __builtin_elementwise_fma(acc[ai][1][m][n], dsu, q.bu[n]);
; #pragma unroll
;                         for (int j = 0; j < 4; ++j) { const float gm = __builtin_fmaxf(gk[j], 7.0f * KP), li = __builtin_amdgcn_fmed3f(up[j], -7.0f, 7.0f);
;                             const float sg = __builtin_amdgcn_rcpf(1.0f + __builtin_amdgcn_exp2f(gm));
;                             h[n * 4 + j] = (gm * sg) * (li * (FP8_SH / KP) + (FP8_SH / KP)); } }
;                     lo[mm] = pk4_fp8(h[0], h[1], h[2], h[3]); hi[mm] = pk4_fp8(h[4], h[5], h[6], h[7]); }
.LBB0_739:
	v_mov_b32_e32 v11, v0
	v_mov_b32_e32 v43, v42
	v_readfirstlane_b32 s19, v11
	v_mov_b32_e32 v47, v46
	s_ashr_i32 s27, s19, 2
	v_mov_b32_e32 v44, v42
	v_mov_b32_e32 v45, v42
	v_mov_b32_e32 v48, v46
	v_mov_b32_e32 v49, v46
	v_mov_b64_e32 v[2:3], v[46:47]
	v_mov_b64_e32 v[6:7], v[42:43]
	v_pk_mul_f32 v[18:19], v[78:79], s[16:17] op_sel_hi:[1,0]
	s_lshl_b32 s21, s38, 8
	s_andn2_b32 s27, s27, 63
	v_mov_b64_e32 v[4:5], v[48:49]
	v_mov_b64_e32 v[8:9], v[44:45]
	s_add_i32 s27, s27, s21
	v_and_or_b32 v10, v11, 31, s27
	v_pk_fma_f32 v[20:21], v[178:179], v[6:7], v[18:19]
	v_lshrrev_b32_e32 v11, 1, v11
	v_max_f32_e32 v23, 0xc1898193, v20
	v_and_b32_e32 v186, 16, v11
	v_exp_f32_e32 v11, v23
	v_max_f32_e32 v21, 0xc1898193, v21
	v_pk_fma_f32 v[28:29], v[182:183], v[2:3], v[38:39]
	v_pk_mul_f32 v[16:17], v[80:81], s[16:17] op_sel_hi:[1,0]
	v_add_f32_e32 v11, 1.0, v11
	v_rcp_f32_e32 v189, v11
	v_exp_f32_e32 v11, v21
	v_med3_f32 v22, v28, s94, v202
	v_pk_fma_f32 v[24:25], v[180:181], v[8:9], v[16:17]
	v_pk_mul_f32 v[22:23], v[22:23], v[188:189]
	v_add_f32_e32 v11, 1.0, v11
	v_sub_f32_e32 v20, 0xbfd083aa, v22
	v_mul_f32_e32 v30, v20, v23
	v_max_f32_e32 v23, 0xc1898193, v24
	v_rcp_f32_e32 v189, v11
	v_exp_f32_e32 v11, v23
	v_med3_f32 v20, v29, s94, v202
	v_max_f32_e32 v25, 0xc1898193, v25
	v_pk_mul_f32 v[20:21], v[20:21], v[188:189]
	v_add_f32_e32 v11, 1.0, v11
	v_rcp_f32_e32 v189, v11
	v_exp_f32_e32 v11, v25
	v_pk_fma_f32 v[26:27], v[184:185], v[4:5], v[40:41]
	v_sub_f32_e32 v20, 0xbfd083aa, v20
	v_med3_f32 v22, v26, s94, v202
	v_add_f32_e32 v11, 1.0, v11
	v_mul_f32_e32 v31, v20, v21
	v_pk_mul_f32 v[20:21], v[22:23], v[188:189]
	v_rcp_f32_e32 v189, v11
	v_sub_f32_e32 v11, 0xbfd083aa, v20
	v_med3_f32 v24, v27, s94, v202
	v_mul_f32_e32 v11, v11, v21
	v_pk_mul_f32 v[20:21], v[24:25], v[188:189]
	v_pk_mul_f32 v[14:15], v[74:75], s[16:17] op_sel_hi:[1,0]
	v_sub_f32_e32 v20, 0xbfd083aa, v20
	v_mul_f32_e32 v32, v20, v21
	v_pk_fma_f32 v[20:21], v[170:171], v[6:7], v[14:15]
	v_pk_fma_f32 v[28:29], v[174:175], v[2:3], v[34:35]
	v_max_f32_e32 v23, 0xc1898193, v20
	v_exp_f32_e32 v20, v23
	v_max_f32_e32 v21, 0xc1898193, v21
	v_med3_f32 v22, v28, s94, v202
	v_pk_mul_f32 v[12:13], v[76:77], s[16:17] op_sel_hi:[1,0]
	v_add_f32_e32 v20, 1.0, v20
	v_rcp_f32_e32 v189, v20
	v_exp_f32_e32 v20, v21
	v_pk_fma_f32 v[24:25], v[172:173], v[8:9], v[12:13]
	v_pk_fma_f32 v[26:27], v[176:177], v[4:5], v[36:37]
	v_pk_mul_f32 v[22:23], v[22:23], v[188:189]
	v_add_f32_e32 v20, 1.0, v20
	v_sub_f32_e32 v22, 0xbfd083aa, v22
	v_mul_f32_e32 v28, v22, v23
	v_max_f32_e32 v23, 0xc1898193, v24
	v_exp_f32_e32 v22, v23
	v_rcp_f32_e32 v189, v20
	v_med3_f32 v20, v29, s94, v202
	v_max_f32_e32 v25, 0xc1898193, v25
	v_add_f32_e32 v22, 1.0, v22
	v_pk_mul_f32 v[20:21], v[20:21], v[188:189]
	v_rcp_f32_e32 v189, v22
	v_exp_f32_e32 v24, v25
	v_sub_f32_e32 v20, 0xbfd083aa, v20
	v_med3_f32 v22, v26, s94, v202
	v_mul_f32_e32 v29, v20, v21
	v_pk_mul_f32 v[20:21], v[22:23], v[188:189]
	v_add_f32_e32 v22, 1.0, v24
	v_rcp_f32_e32 v189, v22
	v_sub_f32_e32 v20, 0xbfd083aa, v20
	v_mul_f32_e32 v26, v20, v21
	v_mov_b32_e32 v21, v187
	v_med3_f32 v24, v27, s94, v202
	v_cvt_pk_fp8_f32 v21, v28, v29
	v_pk_mul_f32 v[22:23], v[24:25], v[188:189]
	v_mov_b32_e32 v20, v187
	v_cvt_pk_fp8_f32 v20, v30, v31
	v_sub_f32_e32 v22, 0xbfd083aa, v22
	v_mul_f32_e32 v22, v22, v23
	v_cvt_pk_fp8_f32 v21, v26, v22 op_sel:[0,0,1]
	v_pk_fma_f32 v[22:23], v[162:163], v[6:7], v[18:19]
	v_cvt_pk_fp8_f32 v20, v11, v32 op_sel:[0,0,1]
	v_max_f32_e32 v25, 0xc1898193, v22
	v_exp_f32_e32 v11, v25
	v_max_f32_e32 v23, 0xc1898193, v23
	v_pk_fma_f32 v[30:31], v[166:167], v[2:3], v[38:39]
	v_pk_fma_f32 v[26:27], v[164:165], v[8:9], v[16:17]
	v_add_f32_e32 v11, 1.0, v11
	v_rcp_f32_e32 v189, v11
	v_exp_f32_e32 v11, v23
	v_med3_f32 v24, v30, s94, v202
	v_max_f32_e32 v27, 0xc1898193, v27
	v_pk_mul_f32 v[24:25], v[24:25], v[188:189]
	v_add_f32_e32 v11, 1.0, v11
	v_sub_f32_e32 v22, 0xbfd083aa, v24
	v_mul_f32_e32 v32, v22, v25
	v_max_f32_e32 v25, 0xc1898193, v26
	v_rcp_f32_e32 v189, v11
	v_exp_f32_e32 v11, v25
	v_med3_f32 v22, v31, s94, v202
	v_pk_fma_f32 v[28:29], v[168:169], v[4:5], v[40:41]
	v_pk_mul_f32 v[22:23], v[22:23], v[188:189]
	v_add_f32_e32 v11, 1.0, v11
	v_rcp_f32_e32 v189, v11
	v_exp_f32_e32 v11, v27
	v_sub_f32_e32 v22, 0xbfd083aa, v22
	v_med3_f32 v24, v28, s94, v202
	v_mul_f32_e32 v33, v22, v23
	v_add_f32_e32 v11, 1.0, v11
	v_pk_mul_f32 v[22:23], v[24:25], v[188:189]
	v_rcp_f32_e32 v189, v11
	v_sub_f32_e32 v11, 0xbfd083aa, v22
	v_med3_f32 v26, v29, s94, v202
	v_mul_f32_e32 v11, v11, v23
	v_pk_mul_f32 v[22:23], v[26:27], v[188:189]
	v_pk_fma_f32 v[30:31], v[158:159], v[2:3], v[34:35]
	v_sub_f32_e32 v22, 0xbfd083aa, v22
	v_mul_f32_e32 v43, v22, v23
	v_pk_fma_f32 v[22:23], v[154:155], v[6:7], v[14:15]
	v_med3_f32 v24, v30, s94, v202
	v_max_f32_e32 v25, 0xc1898193, v22
	v_exp_f32_e32 v22, v25
	v_max_f32_e32 v23, 0xc1898193, v23
	v_pk_fma_f32 v[26:27], v[156:157], v[8:9], v[12:13]
	v_pk_fma_f32 v[28:29], v[160:161], v[4:5], v[36:37]
	v_add_f32_e32 v22, 1.0, v22
	v_rcp_f32_e32 v189, v22
	v_exp_f32_e32 v22, v23
	v_max_f32_e32 v27, 0xc1898193, v27
	s_lshr_b32 s19, s19, 1
	v_pk_mul_f32 v[24:25], v[24:25], v[188:189]
	v_add_f32_e32 v22, 1.0, v22
	v_sub_f32_e32 v24, 0xbfd083aa, v24
	v_mul_f32_e32 v30, v24, v25
	v_max_f32_e32 v25, 0xc1898193, v26
	v_exp_f32_e32 v24, v25
	v_rcp_f32_e32 v189, v22
	v_med3_f32 v22, v31, s94, v202
	v_exp_f32_e32 v26, v27
	v_add_f32_e32 v24, 1.0, v24
	v_pk_mul_f32 v[22:23], v[22:23], v[188:189]
	v_rcp_f32_e32 v189, v24
	v_sub_f32_e32 v22, 0xbfd083aa, v22
	v_med3_f32 v24, v28, s94, v202
	v_mul_f32_e32 v31, v22, v23
; __device__ __forceinline__ unsigned pk4_fp8(float a, float b, float c, float d) { int v = 0; v = __builtin_amdgcn_cvt_pk_fp8_f32(a, b, v, false); v = __builtin_amdgcn_cvt_pk_fp8_f32(c, d, v, true); return (unsigned)v; }
;     __device__ __forceinline__ void operator()(const f32x4 (&acc)[2][2][4][2], const pg8::Unit& u, const Pre& q, int wr, int wc, int fr, int fq) const {
;     ...
;             for (int mp = 0; mp < 2; ++mp) { unsigned lo[2], hi[2];
; #pragma unroll
;                 for (int mm = 0; mm < 2; ++mm) { const int m = 2 * mp + mm; float h[8];
; #pragma unroll
;                     for (int n = 0; n < 2; ++n) { const f32x4 gk = __builtin_elementwise_fma(acc[ai][0][m][n], dsk, q.bg[n]), up = __builtin_elementwise_fma(acc[ai][1][m][n], dsu, q.bu[n]);
; #pragma unroll
;                         for (int j = 0; j < 4; ++j) { const float gm = __builtin_fmaxf(gk[j], 7.0f * KP), li = __builtin_amdgcn_fmed3f(up[j], -7.0f, 7.0f);
;                             const float sg = __builtin_amdgcn_rcpf(1.0f + __builtin_amdgcn_exp2f(gm));
;                             h[n * 4 + j] = (gm * sg) * (li * (FP8_SH / KP) + (FP8_SH / KP)); } }
;                     lo[mm] = pk4_fp8(h[0], h[1], h[2], h[3]); hi[mm] = pk4_fp8(h[4], h[5], h[6], h[7]); }
;                 const v2u r0 = __builtin_amdgcn_permlane16_swap(lo[0], lo[1], false, false), r1 = __builtin_amdgcn_permlane16_swap(hi[0], hi[1], false, false);
;                 unsigned char* rowp = hb + (size_t)(row0 + ai * 128 + (2 * mp + (fq & 1)) * 16) * FF + f0w + 16 * (fq >> 1);
;                 *(v4u*)rowp = (v4u){r0.x, r1.x, r0.y, r1.y}; }
	v_pk_mul_f32 v[22:23], v[24:25], v[188:189]
	v_add_f32_e32 v24, 1.0, v26
	v_rcp_f32_e32 v189, v24
	v_sub_f32_e32 v22, 0xbfd083aa, v22
	v_mul_f32_e32 v28, v22, v23
	v_mov_b32_e32 v22, v187
	v_cvt_pk_fp8_f32 v22, v32, v33
	v_mov_b32_e32 v23, v187
	v_med3_f32 v26, v29, s94, v202
	v_cvt_pk_fp8_f32 v23, v30, v31
	v_pk_mul_f32 v[24:25], v[26:27], v[188:189]
	v_cvt_pk_fp8_f32 v22, v11, v43 op_sel:[0,0,1]
	v_sub_f32_e32 v24, 0xbfd083aa, v24
	v_mul_f32_e32 v11, v24, v25
	s_lshl_b32 s21, s26, 7
	s_and_b32 s19, s19, 0x60
	v_cvt_pk_fp8_f32 v23, v28, v11 op_sel:[0,0,1]
	v_ashrrev_i32_e32 v11, 31, v10
	s_or_b32 s26, s19, s21
	v_lshlrev_b64 v[24:25], 11, v[10:11]
	s_ashr_i32 s27, s26, 31
	v_lshl_add_u64 v[24:25], s[12:13], 0, v[24:25]
	v_lshl_add_u64 v[24:25], v[24:25], 0, s[26:27]
	v_permlane16_swap_b32_e32 v20, v22
	v_permlane16_swap_b32_e32 v21, v23
	v_lshl_add_u64 v[24:25], v[24:25], 0, v[186:187]
	global_store_dwordx4 v[24:25], v[20:23], off
	v_pk_fma_f32 v[28:29], v[150:151], v[2:3], v[38:39]
	v_pk_fma_f32 v[24:25], v[148:149], v[8:9], v[16:17]
	v_pk_fma_f32 v[20:21], v[146:147], v[6:7], v[18:19]
	v_med3_f32 v22, v28, s94, v202
	v_max_f32_e32 v23, 0xc1898193, v20
	v_exp_f32_e32 v11, v23
	v_max_f32_e32 v21, 0xc1898193, v21
	v_max_f32_e32 v25, 0xc1898193, v25
	v_pk_fma_f32 v[26:27], v[152:153], v[4:5], v[40:41]
	v_add_f32_e32 v11, 1.0, v11
	v_rcp_f32_e32 v189, v11
	v_exp_f32_e32 v11, v21
	s_andn2_b64 vcc, exec, s[2:3]
	s_mov_b64 s[2:3], -1
	v_pk_mul_f32 v[22:23], v[22:23], v[188:189]
	v_add_f32_e32 v11, 1.0, v11
	v_sub_f32_e32 v20, 0xbfd083aa, v22
	v_mul_f32_e32 v30, v20, v23
	v_max_f32_e32 v23, 0xc1898193, v24
	v_rcp_f32_e32 v189, v11
	v_exp_f32_e32 v11, v23
	v_med3_f32 v20, v29, s94, v202
	v_med3_f32 v22, v26, s94, v202
	v_pk_mul_f32 v[20:21], v[20:21], v[188:189]
	v_add_f32_e32 v11, 1.0, v11
	v_rcp_f32_e32 v189, v11
	v_exp_f32_e32 v11, v25
	v_sub_f32_e32 v20, 0xbfd083aa, v20
	v_mul_f32_e32 v31, v20, v21
	v_pk_mul_f32 v[20:21], v[22:23], v[188:189]
	v_add_f32_e32 v11, 1.0, v11
	v_rcp_f32_e32 v189, v11
	v_sub_f32_e32 v11, 0xbfd083aa, v20
	v_med3_f32 v24, v27, s94, v202
	v_mul_f32_e32 v11, v11, v21
	v_pk_mul_f32 v[20:21], v[24:25], v[188:189]
	v_pk_fma_f32 v[28:29], v[142:143], v[2:3], v[34:35]
	v_sub_f32_e32 v20, 0xbfd083aa, v20
	v_mul_f32_e32 v32, v20, v21
	v_pk_fma_f32 v[20:21], v[138:139], v[6:7], v[14:15]
	v_med3_f32 v22, v28, s94, v202
	v_max_f32_e32 v23, 0xc1898193, v20
	v_exp_f32_e32 v20, v23
	v_max_f32_e32 v21, 0xc1898193, v21
	v_pk_fma_f32 v[24:25], v[140:141], v[8:9], v[12:13]
	v_pk_fma_f32 v[26:27], v[144:145], v[4:5], v[36:37]
	v_add_f32_e32 v20, 1.0, v20
	v_rcp_f32_e32 v189, v20
	v_exp_f32_e32 v20, v21
	v_max_f32_e32 v25, 0xc1898193, v25
	v_pk_mul_f32 v[22:23], v[22:23], v[188:189]
	s_nop 0
	v_sub_f32_e32 v22, 0xbfd083aa, v22
	v_mul_f32_e32 v28, v22, v23
	v_max_f32_e32 v23, 0xc1898193, v24
	v_add_f32_e32 v20, 1.0, v20
	v_exp_f32_e32 v22, v23
	v_rcp_f32_e32 v189, v20
	v_med3_f32 v20, v29, s94, v202
	v_exp_f32_e32 v24, v25
	v_add_f32_e32 v22, 1.0, v22
	v_pk_mul_f32 v[20:21], v[20:21], v[188:189]
	v_rcp_f32_e32 v189, v22
	v_sub_f32_e32 v20, 0xbfd083aa, v20
	v_med3_f32 v22, v26, s94, v202
	v_mul_f32_e32 v29, v20, v21
	v_pk_mul_f32 v[20:21], v[22:23], v[188:189]
	v_add_f32_e32 v22, 1.0, v24
	v_rcp_f32_e32 v189, v22
	v_sub_f32_e32 v20, 0xbfd083aa, v20
	v_mul_f32_e32 v26, v20, v21
	v_mov_b32_e32 v21, v187
	v_med3_f32 v24, v27, s94, v202
	v_cvt_pk_fp8_f32 v21, v28, v29
	v_pk_mul_f32 v[22:23], v[24:25], v[188:189]
	v_mov_b32_e32 v20, v187
	v_cvt_pk_fp8_f32 v20, v30, v31
	v_sub_f32_e32 v22, 0xbfd083aa, v22
	v_mul_f32_e32 v22, v22, v23
	v_cvt_pk_fp8_f32 v21, v26, v22 op_sel:[0,0,1]
	v_pk_fma_f32 v[22:23], v[130:131], v[6:7], v[18:19]
	v_cvt_pk_fp8_f32 v20, v11, v32 op_sel:[0,0,1]
	v_max_f32_e32 v25, 0xc1898193, v22
	v_exp_f32_e32 v11, v25
	v_max_f32_e32 v23, 0xc1898193, v23
	v_pk_fma_f32 v[30:31], v[134:135], v[2:3], v[38:39]
	v_pk_fma_f32 v[26:27], v[132:133], v[8:9], v[16:17]
	v_add_f32_e32 v11, 1.0, v11
	v_rcp_f32_e32 v189, v11
	v_exp_f32_e32 v11, v23
	v_med3_f32 v24, v30, s94, v202
	v_max_f32_e32 v27, 0xc1898193, v27
	v_pk_mul_f32 v[24:25], v[24:25], v[188:189]
	v_add_f32_e32 v11, 1.0, v11
	v_sub_f32_e32 v22, 0xbfd083aa, v24
	v_mul_f32_e32 v32, v22, v25
	v_max_f32_e32 v25, 0xc1898193, v26
	v_rcp_f32_e32 v189, v11
	v_exp_f32_e32 v11, v25
	v_med3_f32 v22, v31, s94, v202
	v_pk_fma_f32 v[28:29], v[136:137], v[4:5], v[40:41]
	v_pk_mul_f32 v[22:23], v[22:23], v[188:189]
	v_add_f32_e32 v11, 1.0, v11
	v_rcp_f32_e32 v189, v11
	v_exp_f32_e32 v11, v27
	v_sub_f32_e32 v22, 0xbfd083aa, v22
	v_med3_f32 v24, v28, s94, v202
	v_mul_f32_e32 v33, v22, v23
	v_add_f32_e32 v11, 1.0, v11
	v_pk_mul_f32 v[22:23], v[24:25], v[188:189]
	v_rcp_f32_e32 v189, v11
	v_sub_f32_e32 v11, 0xbfd083aa, v22
	v_med3_f32 v26, v29, s94, v202
	v_mul_f32_e32 v11, v11, v23
	v_pk_mul_f32 v[22:23], v[26:27], v[188:189]
	v_pk_fma_f32 v[30:31], v[126:127], v[2:3], v[34:35]
	v_sub_f32_e32 v22, 0xbfd083aa, v22
	v_mul_f32_e32 v43, v22, v23
	v_pk_fma_f32 v[22:23], v[122:123], v[6:7], v[14:15]
	v_med3_f32 v24, v30, s94, v202
	v_max_f32_e32 v25, 0xc1898193, v22
	v_exp_f32_e32 v22, v25
	v_max_f32_e32 v23, 0xc1898193, v23
	v_pk_fma_f32 v[26:27], v[124:125], v[8:9], v[12:13]
	v_pk_fma_f32 v[28:29], v[128:129], v[4:5], v[36:37]
	v_add_f32_e32 v22, 1.0, v22
	v_rcp_f32_e32 v189, v22
	v_exp_f32_e32 v22, v23
	v_max_f32_e32 v27, 0xc1898193, v27
	v_pk_mul_f32 v[24:25], v[24:25], v[188:189]
	s_nop 0
	v_sub_f32_e32 v24, 0xbfd083aa, v24
	v_mul_f32_e32 v30, v24, v25
	v_max_f32_e32 v25, 0xc1898193, v26
	v_add_f32_e32 v22, 1.0, v22
	v_exp_f32_e32 v24, v25
	v_rcp_f32_e32 v189, v22
	v_med3_f32 v22, v31, s94, v202
; __device__ __forceinline__ unsigned pk4_fp8(float a, float b, float c, float d) { int v = 0; v = __builtin_amdgcn_cvt_pk_fp8_f32(a, b, v, false); v = __builtin_amdgcn_cvt_pk_fp8_f32(c, d, v, true); return (unsigned)v; }
;     __device__ __forceinline__ void operator()(const f32x4 (&acc)[2][2][4][2], const pg8::Unit& u, const Pre& q, int wr, int wc, int fr, int fq) const {
;     ...
;             for (int mp = 0; mp < 2; ++mp) { unsigned lo[2], hi[2];
; #pragma unroll
;                 for (int mm = 0; mm < 2; ++mm) { const int m = 2 * mp + mm; float h[8];
; #pragma unroll
;                     for (int n = 0; n < 2; ++n) { const f32x4 gk = __builtin_elementwise_fma(acc[ai][0][m][n], dsk, q.bg[n]), up = __builtin_elementwise_fma(acc[ai][1][m][n], dsu, q.bu[n]);
; #pragma unroll
;                         for (int j = 0; j < 4; ++j) { const float gm = __builtin_fmaxf(gk[j], 7.0f * KP), li = __builtin_amdgcn_fmed3f(up[j], -7.0f, 7.0f);
;                             const float sg = __builtin_amdgcn_rcpf(1.0f + __builtin_amdgcn_exp2f(gm));
;                             h[n * 4 + j] = (gm * sg) * (li * (FP8_SH / KP) + (FP8_SH / KP)); } }
;                     lo[mm] = pk4_fp8(h[0], h[1], h[2], h[3]); hi[mm] = pk4_fp8(h[4], h[5], h[6], h[7]); }
;                 const v2u r0 = __builtin_amdgcn_permlane16_swap(lo[0], lo[1], false, false), r1 = __builtin_amdgcn_permlane16_swap(hi[0], hi[1], false, false);
;                 unsigned char* rowp = hb + (size_t)(row0 + ai * 128 + (2 * mp + (fq & 1)) * 16) * FF + f0w + 16 * (fq >> 1);
;                 *(v4u*)rowp = (v4u){r0.x, r1.x, r0.y, r1.y}; }
	v_exp_f32_e32 v26, v27
	v_add_f32_e32 v24, 1.0, v24
	v_pk_mul_f32 v[22:23], v[22:23], v[188:189]
	v_rcp_f32_e32 v189, v24
	v_sub_f32_e32 v22, 0xbfd083aa, v22
	v_med3_f32 v24, v28, s94, v202
	v_mul_f32_e32 v31, v22, v23
	v_pk_mul_f32 v[22:23], v[24:25], v[188:189]
	v_add_f32_e32 v24, 1.0, v26
	v_rcp_f32_e32 v189, v24
	v_sub_f32_e32 v22, 0xbfd083aa, v22
	v_mul_f32_e32 v28, v22, v23
	v_mov_b32_e32 v22, v187
	v_cvt_pk_fp8_f32 v22, v32, v33
	v_mov_b32_e32 v23, v187
	v_med3_f32 v26, v29, s94, v202
	v_cvt_pk_fp8_f32 v23, v30, v31
	v_pk_mul_f32 v[24:25], v[26:27], v[188:189]
	v_cvt_pk_fp8_f32 v22, v11, v43 op_sel:[0,0,1]
	v_sub_f32_e32 v24, 0xbfd083aa, v24
	v_mul_f32_e32 v11, v24, v25
	v_or_b32_e32 v24, 32, v10
	v_cvt_pk_fp8_f32 v23, v28, v11 op_sel:[0,0,1]
	v_ashrrev_i32_e32 v25, 31, v24
	v_lshlrev_b64 v[24:25], 11, v[24:25]
	v_lshl_add_u64 v[24:25], s[12:13], 0, v[24:25]
	v_lshl_add_u64 v[24:25], v[24:25], 0, s[26:27]
	v_permlane16_swap_b32_e32 v20, v22
	v_permlane16_swap_b32_e32 v21, v23
	v_lshl_add_u64 v[24:25], v[24:25], 0, v[186:187]
	global_store_dwordx4 v[24:25], v[20:23], off
	v_pk_fma_f32 v[30:31], v[106:107], v[2:3], v[38:39]
	v_pk_fma_f32 v[26:27], v[120:121], v[8:9], v[16:17]
	v_pk_fma_f32 v[22:23], v[118:119], v[6:7], v[18:19]
	v_med3_f32 v24, v30, s94, v202
	v_max_f32_e32 v25, 0xc1898193, v22
	v_exp_f32_e32 v11, v25
	v_max_f32_e32 v23, 0xc1898193, v23
	v_med3_f32 v22, v31, s94, v202
	v_max_f32_e32 v27, 0xc1898193, v27
	v_add_f32_e32 v11, 1.0, v11
	v_rcp_f32_e32 v189, v11
	v_exp_f32_e32 v11, v23
	v_pk_fma_f32 v[28:29], v[108:109], v[4:5], v[40:41]
	v_pk_fma_f32 v[30:31], v[114:115], v[2:3], v[34:35]
	v_pk_mul_f32 v[24:25], v[24:25], v[188:189]
	v_add_f32_e32 v11, 1.0, v11
	v_sub_f32_e32 v21, 0xbfd083aa, v24
	v_mul_f32_e32 v21, v21, v25
	v_max_f32_e32 v25, 0xc1898193, v26
	v_rcp_f32_e32 v189, v11
	v_exp_f32_e32 v11, v25
	v_med3_f32 v24, v28, s94, v202
	v_med3_f32 v26, v29, s94, v202
	v_pk_mul_f32 v[22:23], v[22:23], v[188:189]
	v_add_f32_e32 v11, 1.0, v11
	v_rcp_f32_e32 v189, v11
	v_exp_f32_e32 v11, v27
	v_sub_f32_e32 v22, 0xbfd083aa, v22
	v_mul_f32_e32 v32, v22, v23
	v_pk_mul_f32 v[22:23], v[24:25], v[188:189]
	v_add_f32_e32 v11, 1.0, v11
	v_rcp_f32_e32 v189, v11
	v_sub_f32_e32 v11, 0xbfd083aa, v22
	v_mul_f32_e32 v11, v11, v23
	v_med3_f32 v24, v30, s94, v202
	v_pk_mul_f32 v[22:23], v[26:27], v[188:189]
	v_pk_fma_f32 v[26:27], v[112:113], v[8:9], v[12:13]
	v_sub_f32_e32 v22, 0xbfd083aa, v22
	v_mul_f32_e32 v33, v22, v23
	v_pk_fma_f32 v[22:23], v[110:111], v[6:7], v[14:15]
	v_max_f32_e32 v27, 0xc1898193, v27
	v_max_f32_e32 v25, 0xc1898193, v22
	v_exp_f32_e32 v22, v25
	v_max_f32_e32 v23, 0xc1898193, v23
	v_pk_fma_f32 v[28:29], v[116:117], v[4:5], v[36:37]
	v_add_u32_e32 v20, 0x80, v10
	v_add_f32_e32 v22, 1.0, v22
	v_rcp_f32_e32 v189, v22
	v_exp_f32_e32 v22, v23
	v_pk_mul_f32 v[24:25], v[24:25], v[188:189]
	s_nop 0
	v_sub_f32_e32 v24, 0xbfd083aa, v24
	v_mul_f32_e32 v30, v24, v25
	v_max_f32_e32 v25, 0xc1898193, v26
	v_add_f32_e32 v22, 1.0, v22
	v_exp_f32_e32 v24, v25
	v_rcp_f32_e32 v189, v22
	v_med3_f32 v22, v31, s94, v202
	v_exp_f32_e32 v26, v27
	v_add_f32_e32 v24, 1.0, v24
	v_pk_mul_f32 v[22:23], v[22:23], v[188:189]
	v_rcp_f32_e32 v189, v24
	v_sub_f32_e32 v22, 0xbfd083aa, v22
	v_med3_f32 v24, v28, s94, v202
	v_mul_f32_e32 v31, v22, v23
	v_pk_mul_f32 v[22:23], v[24:25], v[188:189]
	v_add_f32_e32 v24, 1.0, v26
	v_rcp_f32_e32 v189, v24
	v_sub_f32_e32 v22, 0xbfd083aa, v22
	v_mul_f32_e32 v28, v22, v23
	v_med3_f32 v26, v29, s94, v202
	v_mov_b32_e32 v22, v187
	v_pk_mul_f32 v[24:25], v[26:27], v[188:189]
	v_cvt_pk_fp8_f32 v22, v21, v32
	v_sub_f32_e32 v21, 0xbfd083aa, v24
	v_mul_f32_e32 v21, v21, v25
	v_pk_fma_f32 v[24:25], v[98:99], v[6:7], v[18:19]
	v_cvt_pk_fp8_f32 v22, v11, v33 op_sel:[0,0,1]
	v_max_f32_e32 v27, 0xc1898193, v24
	v_exp_f32_e32 v11, v27
	v_mov_b32_e32 v23, v187
	v_cvt_pk_fp8_f32 v23, v30, v31
	v_max_f32_e32 v25, 0xc1898193, v25
	v_add_f32_e32 v11, 1.0, v11
	v_rcp_f32_e32 v189, v11
	v_pk_fma_f32 v[32:33], v[102:103], v[2:3], v[38:39]
	v_exp_f32_e32 v11, v25
	v_med3_f32 v26, v32, s94, v202
	v_pk_mul_f32 v[26:27], v[26:27], v[188:189]
	v_cvt_pk_fp8_f32 v23, v28, v21 op_sel:[0,0,1]
	v_pk_fma_f32 v[28:29], v[100:101], v[8:9], v[16:17]
	v_sub_f32_e32 v21, 0xbfd083aa, v26
	v_mul_f32_e32 v21, v21, v27
	v_add_f32_e32 v11, 1.0, v11
	v_max_f32_e32 v27, 0xc1898193, v28
	v_rcp_f32_e32 v189, v11
	v_exp_f32_e32 v11, v27
	v_med3_f32 v24, v33, s94, v202
	v_max_f32_e32 v29, 0xc1898193, v29
	v_pk_mul_f32 v[24:25], v[24:25], v[188:189]
	v_add_f32_e32 v11, 1.0, v11
	v_rcp_f32_e32 v189, v11
	v_exp_f32_e32 v11, v29
	v_pk_fma_f32 v[30:31], v[104:105], v[4:5], v[40:41]
	v_sub_f32_e32 v24, 0xbfd083aa, v24
	v_med3_f32 v26, v30, s94, v202
	v_add_f32_e32 v11, 1.0, v11
	v_mul_f32_e32 v43, v24, v25
	v_pk_mul_f32 v[24:25], v[26:27], v[188:189]
	v_rcp_f32_e32 v189, v11
	v_sub_f32_e32 v11, 0xbfd083aa, v24
	v_med3_f32 v28, v31, s94, v202
	v_mul_f32_e32 v11, v11, v25
	v_pk_mul_f32 v[24:25], v[28:29], v[188:189]
	v_pk_fma_f32 v[32:33], v[94:95], v[2:3], v[34:35]
	v_sub_f32_e32 v24, 0xbfd083aa, v24
	v_mul_f32_e32 v44, v24, v25
	v_pk_fma_f32 v[24:25], v[90:91], v[6:7], v[14:15]
	v_med3_f32 v26, v32, s94, v202
	v_max_f32_e32 v27, 0xc1898193, v24
	v_exp_f32_e32 v24, v27
	v_max_f32_e32 v25, 0xc1898193, v25
	v_pk_fma_f32 v[28:29], v[92:93], v[8:9], v[12:13]
	v_pk_fma_f32 v[30:31], v[96:97], v[4:5], v[36:37]
	v_add_f32_e32 v24, 1.0, v24
	v_rcp_f32_e32 v189, v24
	v_exp_f32_e32 v24, v25
	v_max_f32_e32 v29, 0xc1898193, v29
	v_pk_mul_f32 v[26:27], v[26:27], v[188:189]
	s_nop 0
	v_sub_f32_e32 v26, 0xbfd083aa, v26
	v_mul_f32_e32 v32, v26, v27
	v_max_f32_e32 v27, 0xc1898193, v28
; __device__ __forceinline__ unsigned pk4_fp8(float a, float b, float c, float d) { int v = 0; v = __builtin_amdgcn_cvt_pk_fp8_f32(a, b, v, false); v = __builtin_amdgcn_cvt_pk_fp8_f32(c, d, v, true); return (unsigned)v; }
;     __device__ __forceinline__ void operator()(const f32x4 (&acc)[2][2][4][2], const pg8::Unit& u, const Pre& q, int wr, int wc, int fr, int fq) const {
;     ...
;             for (int mp = 0; mp < 2; ++mp) { unsigned lo[2], hi[2];
; #pragma unroll
;                 for (int mm = 0; mm < 2; ++mm) { const int m = 2 * mp + mm; float h[8];
; #pragma unroll
;                     for (int n = 0; n < 2; ++n) { const f32x4 gk = __builtin_elementwise_fma(acc[ai][0][m][n], dsk, q.bg[n]), up = __builtin_elementwise_fma(acc[ai][1][m][n], dsu, q.bu[n]);
; #pragma unroll
;                         for (int j = 0; j < 4; ++j) { const float gm = __builtin_fmaxf(gk[j], 7.0f * KP), li = __builtin_amdgcn_fmed3f(up[j], -7.0f, 7.0f);
;                             const float sg = __builtin_amdgcn_rcpf(1.0f + __builtin_amdgcn_exp2f(gm));
;                             h[n * 4 + j] = (gm * sg) * (li * (FP8_SH / KP) + (FP8_SH / KP)); } }
;                     lo[mm] = pk4_fp8(h[0], h[1], h[2], h[3]); hi[mm] = pk4_fp8(h[4], h[5], h[6], h[7]); }
;                 const v2u r0 = __builtin_amdgcn_permlane16_swap(lo[0], lo[1], false, false), r1 = __builtin_amdgcn_permlane16_swap(hi[0], hi[1], false, false);
;                 unsigned char* rowp = hb + (size_t)(row0 + ai * 128 + (2 * mp + (fq & 1)) * 16) * FF + f0w + 16 * (fq >> 1);
;                 *(v4u*)rowp = (v4u){r0.x, r1.x, r0.y, r1.y}; }
	v_add_f32_e32 v24, 1.0, v24
	v_exp_f32_e32 v26, v27
	v_rcp_f32_e32 v189, v24
	v_med3_f32 v24, v33, s94, v202
	v_exp_f32_e32 v28, v29
	v_add_f32_e32 v26, 1.0, v26
	v_pk_mul_f32 v[24:25], v[24:25], v[188:189]
	v_rcp_f32_e32 v189, v26
	v_sub_f32_e32 v24, 0xbfd083aa, v24
	v_med3_f32 v26, v30, s94, v202
	v_mul_f32_e32 v33, v24, v25
	v_pk_mul_f32 v[24:25], v[26:27], v[188:189]
	v_add_f32_e32 v26, 1.0, v28
	v_rcp_f32_e32 v189, v26
	v_sub_f32_e32 v24, 0xbfd083aa, v24
	v_mul_f32_e32 v30, v24, v25
	v_mov_b32_e32 v24, v187
	v_cvt_pk_fp8_f32 v24, v21, v43
	v_mov_b32_e32 v25, v187
	v_med3_f32 v28, v31, s94, v202
	v_cvt_pk_fp8_f32 v25, v32, v33
	v_pk_mul_f32 v[26:27], v[28:29], v[188:189]
	v_cvt_pk_fp8_f32 v24, v11, v44 op_sel:[0,0,1]
	v_sub_f32_e32 v21, 0xbfd083aa, v26
	v_mul_f32_e32 v11, v21, v27
	v_cvt_pk_fp8_f32 v25, v30, v11 op_sel:[0,0,1]
	v_ashrrev_i32_e32 v21, 31, v20
	v_lshlrev_b64 v[20:21], 11, v[20:21]
	v_lshl_add_u64 v[20:21], s[12:13], 0, v[20:21]
	v_lshl_add_u64 v[20:21], v[20:21], 0, s[26:27]
	v_permlane16_swap_b32_e32 v22, v24
	v_permlane16_swap_b32_e32 v23, v25
	v_lshl_add_u64 v[20:21], v[20:21], 0, v[186:187]
	global_store_dwordx4 v[20:21], v[22:25], off
	v_pk_fma_f32 v[20:21], v[82:83], v[6:7], v[18:19]
	v_pk_fma_f32 v[28:29], v[86:87], v[2:3], v[38:39]
	v_max_f32_e32 v23, 0xc1898193, v20
	v_exp_f32_e32 v11, v23
	v_max_f32_e32 v21, 0xc1898193, v21
	v_med3_f32 v22, v28, s94, v202
	v_pk_fma_f32 v[24:25], v[84:85], v[8:9], v[16:17]
	v_add_f32_e32 v11, 1.0, v11
	v_rcp_f32_e32 v189, v11
	v_exp_f32_e32 v11, v21
	v_max_f32_e32 v25, 0xc1898193, v25
	v_pk_fma_f32 v[26:27], v[88:89], v[4:5], v[40:41]
	v_pk_mul_f32 v[22:23], v[22:23], v[188:189]
	v_add_f32_e32 v11, 1.0, v11
	v_sub_f32_e32 v20, 0xbfd083aa, v22
	v_mul_f32_e32 v30, v20, v23
	v_max_f32_e32 v23, 0xc1898193, v24
	v_rcp_f32_e32 v189, v11
	v_exp_f32_e32 v11, v23
	v_med3_f32 v20, v29, s94, v202
	v_med3_f32 v22, v26, s94, v202
	v_pk_mul_f32 v[20:21], v[20:21], v[188:189]
	v_add_f32_e32 v11, 1.0, v11
	v_rcp_f32_e32 v189, v11
	v_exp_f32_e32 v11, v25
	v_sub_f32_e32 v20, 0xbfd083aa, v20
	v_mul_f32_e32 v31, v20, v21
	v_pk_mul_f32 v[20:21], v[22:23], v[188:189]
	v_add_f32_e32 v11, 1.0, v11
	v_rcp_f32_e32 v189, v11
	v_sub_f32_e32 v11, 0xbfd083aa, v20
	v_med3_f32 v24, v27, s94, v202
	v_mul_f32_e32 v11, v11, v21
	v_pk_mul_f32 v[20:21], v[24:25], v[188:189]
	v_pk_fma_f32 v[28:29], v[70:71], v[2:3], v[34:35]
	v_sub_f32_e32 v20, 0xbfd083aa, v20
	v_mul_f32_e32 v32, v20, v21
	v_pk_fma_f32 v[20:21], v[66:67], v[6:7], v[14:15]
	v_med3_f32 v22, v28, s94, v202
	v_max_f32_e32 v23, 0xc1898193, v20
	v_exp_f32_e32 v20, v23
	v_max_f32_e32 v21, 0xc1898193, v21
	v_pk_fma_f32 v[24:25], v[68:69], v[8:9], v[12:13]
	v_pk_fma_f32 v[26:27], v[72:73], v[4:5], v[36:37]
	v_add_f32_e32 v20, 1.0, v20
	v_rcp_f32_e32 v189, v20
	v_exp_f32_e32 v20, v21
	v_max_f32_e32 v25, 0xc1898193, v25
	v_pk_fma_f32 v[18:19], v[58:59], v[6:7], v[18:19]
	v_pk_mul_f32 v[22:23], v[22:23], v[188:189]
	v_add_f32_e32 v20, 1.0, v20
	v_sub_f32_e32 v22, 0xbfd083aa, v22
	v_mul_f32_e32 v28, v22, v23
	v_max_f32_e32 v23, 0xc1898193, v24
	v_exp_f32_e32 v22, v23
	v_rcp_f32_e32 v189, v20
	v_med3_f32 v20, v29, s94, v202
	v_exp_f32_e32 v24, v25
	v_add_f32_e32 v22, 1.0, v22
	v_pk_mul_f32 v[20:21], v[20:21], v[188:189]
	v_rcp_f32_e32 v189, v22
	v_sub_f32_e32 v20, 0xbfd083aa, v20
	v_med3_f32 v22, v26, s94, v202
	v_mul_f32_e32 v29, v20, v21
	v_pk_mul_f32 v[20:21], v[22:23], v[188:189]
	v_add_f32_e32 v22, 1.0, v24
	v_rcp_f32_e32 v189, v22
	v_sub_f32_e32 v20, 0xbfd083aa, v20
	v_mul_f32_e32 v26, v20, v21
	v_mov_b32_e32 v20, v187
	v_med3_f32 v24, v27, s94, v202
	v_cvt_pk_fp8_f32 v20, v30, v31
	v_pk_mul_f32 v[22:23], v[24:25], v[188:189]
	v_mov_b32_e32 v21, v187
	v_sub_f32_e32 v22, 0xbfd083aa, v22
	v_mul_f32_e32 v22, v22, v23
	v_max_f32_e32 v23, 0xc1898193, v18
	v_cvt_pk_fp8_f32 v20, v11, v32 op_sel:[0,0,1]
	v_exp_f32_e32 v11, v23
	v_cvt_pk_fp8_f32 v21, v28, v29
	v_max_f32_e32 v19, 0xc1898193, v19
	v_pk_fma_f32 v[16:17], v[60:61], v[8:9], v[16:17]
	v_add_f32_e32 v11, 1.0, v11
	v_rcp_f32_e32 v189, v11
	v_cvt_pk_fp8_f32 v21, v26, v22 op_sel:[0,0,1]
	v_pk_fma_f32 v[26:27], v[62:63], v[2:3], v[38:39]
	v_exp_f32_e32 v11, v19
	v_med3_f32 v22, v26, s94, v202
	v_pk_mul_f32 v[22:23], v[22:23], v[188:189]
	v_max_f32_e32 v17, 0xc1898193, v17
	v_sub_f32_e32 v18, 0xbfd083aa, v22
	v_mul_f32_e32 v26, v18, v23
	v_add_f32_e32 v11, 1.0, v11
	v_max_f32_e32 v23, 0xc1898193, v16
	v_rcp_f32_e32 v189, v11
	v_exp_f32_e32 v11, v23
	v_med3_f32 v18, v27, s94, v202
	v_pk_fma_f32 v[6:7], v[50:51], v[6:7], v[14:15]
	v_pk_mul_f32 v[18:19], v[18:19], v[188:189]
	v_add_f32_e32 v11, 1.0, v11
	v_rcp_f32_e32 v189, v11
	v_exp_f32_e32 v11, v17
	v_pk_fma_f32 v[24:25], v[64:65], v[4:5], v[40:41]
	v_max_f32_e32 v15, 0xc1898193, v6
	v_sub_f32_e32 v16, 0xbfd083aa, v18
	v_med3_f32 v22, v24, s94, v202
	v_add_f32_e32 v11, 1.0, v11
	v_exp_f32_e32 v6, v15
	v_mul_f32_e32 v27, v16, v19
	v_pk_mul_f32 v[18:19], v[22:23], v[188:189]
	v_rcp_f32_e32 v189, v11
	v_med3_f32 v16, v25, s94, v202
	v_add_f32_e32 v6, 1.0, v6
	v_pk_fma_f32 v[2:3], v[54:55], v[2:3], v[34:35]
	v_pk_mul_f32 v[16:17], v[16:17], v[188:189]
	v_rcp_f32_e32 v189, v6
	v_max_f32_e32 v7, 0xc1898193, v7
	v_med3_f32 v14, v2, s94, v202
	v_exp_f32_e32 v2, v7
	v_pk_fma_f32 v[8:9], v[52:53], v[8:9], v[12:13]
	v_pk_mul_f32 v[12:13], v[14:15], v[188:189]
	v_pk_fma_f32 v[4:5], v[56:57], v[4:5], v[36:37]
	v_sub_f32_e32 v6, 0xbfd083aa, v12
	v_mul_f32_e32 v14, v6, v13
	v_add_f32_e32 v2, 1.0, v2
	v_max_f32_e32 v13, 0xc1898193, v8
	v_rcp_f32_e32 v189, v2
	v_exp_f32_e32 v8, v13
	v_med3_f32 v6, v3, s94, v202
	v_med3_f32 v12, v4, s94, v202
	v_pk_mul_f32 v[2:3], v[6:7], v[188:189]
	v_add_f32_e32 v6, 1.0, v8
	v_max_f32_e32 v7, 0xc1898193, v9
	v_rcp_f32_e32 v189, v6
	v_exp_f32_e32 v6, v7
	v_sub_f32_e32 v2, 0xbfd083aa, v2
	v_mul_f32_e32 v8, v2, v3
	v_pk_mul_f32 v[2:3], v[12:13], v[188:189]
	v_add_f32_e32 v4, 1.0, v6
	v_rcp_f32_e32 v189, v4
	v_mov_b32_e32 v23, v187
	v_sub_f32_e32 v2, 0xbfd083aa, v2
	v_med3_f32 v6, v5, s94, v202
	v_mov_b32_e32 v22, v187
	v_cvt_pk_fp8_f32 v23, v14, v8
	v_mul_f32_e32 v4, v2, v3
	v_pk_mul_f32 v[2:3], v[6:7], v[188:189]
	v_cvt_pk_fp8_f32 v22, v26, v27
	v_sub_f32_e32 v2, 0xbfd083aa, v2
	v_sub_f32_e32 v11, 0xbfd083aa, v18
	v_sub_f32_e32 v16, 0xbfd083aa, v16
	v_mul_f32_e32 v2, v2, v3
	v_mul_f32_e32 v11, v11, v19
	v_mul_f32_e32 v16, v16, v17
	v_cvt_pk_fp8_f32 v23, v4, v2 op_sel:[0,0,1]
	v_add_u32_e32 v2, 0xa0, v10
	v_cvt_pk_fp8_f32 v22, v11, v16 op_sel:[0,0,1]
	v_ashrrev_i32_e32 v3, 31, v2
	v_lshlrev_b64 v[2:3], 11, v[2:3]
	v_lshl_add_u64 v[2:3], s[12:13], 0, v[2:3]
	v_lshl_add_u64 v[2:3], v[2:3], 0, s[26:27]
	v_permlane16_swap_b32_e32 v20, v22
	v_permlane16_swap_b32_e32 v21, v23
	v_lshl_add_u64 v[2:3], v[2:3], 0, v[186:187]
	global_store_dwordx4 v[2:3], v[20:23], off
	s_cbranch_vccnz .LBB0_726
; #define PG8_BAR __builtin_amdgcn_s_barrier()
; template <class Epi, class Sched>
; __device__ __forceinline__ void gemm_phase(LAS unsigned char* lds, const Sched& S, const Epi& E) {
;     ...
;         cur = nxt; cA = nA; cB = nB; crot = nrot; ++ui;
;         E.prefetch(cur, epre);
;         if (wr == 1) PG8_BAR;
;     __device__ __forceinline__ void prefetch(const pg8::Unit& u, Pre& q) const {
;         int tz = threadIdx.x; asm volatile("" : "+v"(tz)); const int wc = (tz >> 6) & 3, fq = (tz >> 4) & 3;
;         const int f0 = u.pn * 128 + wc * 32 + 8 * fq;
; #pragma unroll
;         for (int n = 0; n < 2; ++n) { q.bg[n] = *(const f32x4*)(b_gate + (size_t)u.e * FF + f0 + 4 * n) * KP; q.bu[n] = *(const f32x4*)(b_up + (size_t)u.e * FF + f0 + 4 * n); }
	v_mov_b32_e32 v2, v0
	s_ashr_i32 s21, s20, 31
	v_readlane_b32 s72, v255, 29
	v_lshrrev_b32_e32 v2, 1, v2
	s_lshl_b64 s[2:3], s[20:21], 13
	v_readlane_b32 s76, v255, 33
	v_and_b32_e32 v2, 0x78, v2
	v_readlane_b32 s77, v255, 34
	s_add_u32 s26, s76, s2
	v_lshl_or_b32 v2, s44, 7, v2
	v_readlane_b32 s80, v255, 37
	s_addc_u32 s27, s77, s3
	v_ashrrev_i32_e32 v3, 31, v2
	v_readlane_b32 s81, v255, 38
	s_add_u32 s2, s80, s2
	v_lshlrev_b64 v[2:3], 2, v[2:3]
	s_addc_u32 s3, s81, s3
	v_lshl_add_u64 v[4:5], s[26:27], 0, v[2:3]
	v_lshl_add_u64 v[2:3], s[2:3], 0, v[2:3]
	global_load_dwordx4 v[74:77], v[4:5], off offset:16
	global_load_dwordx4 v[78:81], v[4:5], off
	global_load_dwordx4 v[34:37], v[2:3], off offset:16
	global_load_dwordx4 v[38:41], v[2:3], off
	v_readlane_b32 s2, v255, 53
	v_readlane_b32 s3, v255, 54
	s_andn2_b64 vcc, exec, s[2:3]
	v_readlane_b32 s73, v255, 30
	v_readlane_b32 s74, v255, 31
	v_readlane_b32 s75, v255, 32
	v_readlane_b32 s78, v255, 35
	v_readlane_b32 s79, v255, 36
	v_readlane_b32 s82, v255, 39
	v_readlane_b32 s83, v255, 40
	v_readlane_b32 s84, v255, 41
	v_readlane_b32 s85, v255, 42
	v_readlane_b32 s86, v255, 43
	v_readlane_b32 s87, v255, 44
	s_mov_b32 s100, 0
	s_cbranch_vccnz .LBB0_725
	s_mov_b32 s100, 1
	s_branch .LBB0_725

; #define PG8_STAGE(bufoff, gbase, voff) do { if constexpr (!(Sched::CRIP & 2)) _Pragma("unroll") for (int _i = 0; _i < 2; ++_i) { unsigned _o = (voff)[_i]; asm volatile("" : "+v"(_o)); \
;         __builtin_amdgcn_global_load_lds((const unsigned*)((const char*)(gbase) + _o), (LAS unsigned*)(lds + (bufoff) + ldsw + _i * 8192), 16, 0, 0); } } while (0)
; #define PG8_WAIT_V(n) asm volatile("s_waitcnt vmcnt(" #n ")" ::: "memory")
; #define PG8_BAR __builtin_amdgcn_s_barrier()
; template <class Epi, class Sched>
; __device__ __forceinline__ void gemm_phase(LAS unsigned char* lds, const Sched& S, const Epi& E) {
;     ...
;     PG8_STAGE(PG8_SB(0, 0), cB + PG8_KT(crot, 0), voffB); PG8_STAGE(PG8_SB(0, 1), cB + hstep + PG8_KT(crot, 0), voffB); PG8_STAGE(PG8_SA(0, 0), cA + PG8_KT(crot, 0), vA[0]); PG8_STAGE(PG8_SA(0, 1), cA + PG8_KT(crot, 0), vA[1]);
;     if (wr == 1) PG8_BAR;
;     PG8_WAIT_V(2); PG8_BAR;
;     PG8_STAGE(PG8_SB(1, 0), cB + PG8_KT(crot, 1), voffB); PG8_STAGE(PG8_SA(1, 0), cA + PG8_KT(crot, 1), vA[0]); PG8_STAGE(PG8_SB(1, 1), cB + hstep + PG8_KT(crot, 1), voffB);
;     PG8_WAIT_V(6); PG8_BAR;
.LBB0_801:
	s_add_u32 s6, s88, 0x1000000
	s_addc_u32 s7, s89, 0
	s_lshl_b32 s14, s8, 13
	s_lshl_b32 s8, s24, 7
	s_lshl_b32 s1, s1, 12
	s_addk_i32 s8, 0x80
	s_and_b32 s1, s1, 0x3000
	s_and_b32 s8, s8, 0x780
	s_add_u32 s12, s28, s8
	v_mov_b32_e32 v2, v1
	s_waitcnt vmcnt(2)
	s_barrier
	s_addc_u32 s13, s29, 0
	s_add_i32 m0, s69, 0x18000
	v_lshlrev_b32_e32 v3, 6, v0
	global_load_lds_dwordx4 v2, s[12:13]
	v_mov_b32_e32 v2, v180
	s_add_i32 m0, s69, 0x1a000
	v_and_b32_e32 v3, 0x3c0, v3
	global_load_lds_dwordx4 v2, s[12:13]
	s_add_u32 s12, s26, s8
	s_addc_u32 s13, s27, 0
	v_mov_b32_e32 v2, v181
	s_add_i32 s74, s69, 0x8000
	s_mov_b32 m0, s74
	s_add_i32 s75, s69, 0xa000
	global_load_lds_dwordx4 v2, s[12:13]
	v_mov_b32_e32 v2, v182
	s_mov_b32 m0, s75
	s_add_u32 s8, s9, s8
	global_load_lds_dwordx4 v2, s[12:13]
	v_mov_b32_e32 v2, v1
	s_addc_u32 s9, s10, 0
	s_add_i32 m0, s69, 0x1c000
	v_lshlrev_b32_e32 v5, 2, v0
	global_load_lds_dwordx4 v2, s[8:9]
	v_mov_b32_e32 v2, v180
	s_add_i32 m0, s69, 0x1e000
	v_and_b32_e32 v5, 32, v5
	global_load_lds_dwordx4 v2, s[8:9]
	v_and_b32_e32 v2, 48, v0
	v_or_b32_e32 v4, v3, v2
	s_waitcnt vmcnt(0)
	s_cmpk_lt_u32 s0, 0x100
	v_bitop3_b32 v2, v3, v5, v2 bitop3:0x36
	v_bitop3_b32 v3, s14, v4, v5 bitop3:0xf6
	s_cselect_b64 s[8:9], -1, 0
	s_add_i32 s0, 0, 0x27d80
	v_or_b32_e32 v186, s1, v2
	s_ashr_i32 s76, s96, 31
	v_mov_b32_e32 v187, s0
	s_add_i32 s77, 0, 0x10000
	s_add_i32 s78, 0, 0x14000
	v_add_u32_e32 v188, 0, v3
	v_mov_b32_e32 v179, 0
	s_mov_b32 s10, 0x3a800000
	s_mov_b32 s79, 0xc3e00000
	v_mov_b32_e32 v189, 0x43e00000
	s_mov_b64 s[94:95], s[28:29]
	s_mov_b64 s[92:93], s[26:27]
	v_readlane_b32 s38, v255, 28
	s_barrier
	s_mov_b32 s100, 0
	s_branch .LBB0_804

; __device__ __forceinline__ float sat8(float x) { return __builtin_amdgcn_fmed3f(x, -448.0f, 448.0f); }
; __device__ __forceinline__ unsigned pk4_fp8(float a, float b, float c, float d) { int v = 0; v = __builtin_amdgcn_cvt_pk_fp8_f32(a, b, v, false); v = __builtin_amdgcn_cvt_pk_fp8_f32(c, d, v, true); return (unsigned)v; }
;     __device__ __forceinline__ void operator()(const f32x4 (&acc)[2][2][4][2], const pg8::Unit& u, const Pre& q, int wr, int wc, int fr, int fq) const {
;         const int rl0 = wr * 64 + fr, colw = u.pn * 256 + wc * 32;
;         constexpr float DS = 1.0f / (FP8_SH * FP8_SW);
; #pragma unroll
;         for (int ai = 0; ai < 2; ++ai)
; #pragma unroll
;             for (int mp = 0; mp < 2; ++mp)
; #pragma unroll
;                 for (int bj = 0; bj < 2; ++bj) { unsigned lo[2], hi[2];
; #pragma unroll
;                     for (int mm = 0; mm < 2; ++mm) { const int m = 2 * mp + mm; const float gt = q.gt[ai][m] * FP8_SY;
;                         const f32x4 v0 = (acc[ai][bj][m][0] * DS + q.bv[bj][0]) * gt, v1 = (acc[ai][bj][m][1] * DS + q.bv[bj][1]) * gt;
;                         lo[mm] = pk4_fp8(sat8(v0[0]), sat8(v0[1]), sat8(v0[2]), sat8(v0[3])); hi[mm] = pk4_fp8(sat8(v1[0]), sat8(v1[1]), sat8(v1[2]), sat8(v1[3])); }
;                     const v2u r0 = __builtin_amdgcn_permlane16_swap(lo[0], lo[1], false, false), r1 = __builtin_amdgcn_permlane16_swap(hi[0], hi[1], false, false);
;                     unsigned char* rowp = y2 + (size_t)(u.pm * 256 + rl0 + ai * 128 + (2 * mp + (fq & 1)) * 16) * D + colw + bj * 128 + 16 * (fq >> 1);
;                     *(v4u*)rowp = (v4u){r0.x, r1.x, r0.y, r1.y}; }
.LBB0_810:
	v_mov_b32_e32 v3, v0
	s_lshl_b32 s24, s24, 8
	v_readfirstlane_b32 s15, v3
	s_ashr_i32 s17, s15, 2
	s_lshr_b32 s15, s15, 1
	s_and_b32 s15, s15, 0x60
	s_andn2_b32 s17, s17, 63
	s_or_b32 s24, s15, s24
	s_lshl_b32 s15, s22, 8
	s_add_i32 s17, s17, s15
	v_and_or_b32 v2, v3, 31, s17
	v_lshrrev_b32_e32 v3, 1, v3
	s_waitcnt vmcnt(8)
	v_mul_f32_e32 v10, 0x42000000, v197
	v_pk_fma_f32 v[4:5], v[176:177], s[10:11], v[48:49] op_sel_hi:[1,0,1]
	v_pk_fma_f32 v[6:7], v[174:175], s[10:11], v[46:47] op_sel_hi:[1,0,1]
	v_and_b32_e32 v178, 16, v3
	v_ashrrev_i32_e32 v3, 31, v2
	v_pk_mul_f32 v[4:5], v[10:11], v[4:5] op_sel_hi:[0,1]
	v_pk_mul_f32 v[6:7], v[10:11], v[6:7] op_sel_hi:[0,1]
	v_pk_fma_f32 v[14:15], v[170:171], s[10:11], v[42:43] op_sel_hi:[1,0,1]
	v_lshlrev_b64 v[8:9], 11, v[2:3]
	v_pk_fma_f32 v[12:13], v[172:173], s[10:11], v[44:45] op_sel_hi:[1,0,1]
	v_pk_mul_f32 v[14:15], v[10:11], v[14:15] op_sel_hi:[0,1]
	v_med3_f32 v3, v6, s79, v189
	v_med3_f32 v6, v7, s79, v189
	v_med3_f32 v7, v4, s79, v189
	v_mov_b32_e32 v4, v179
	v_pk_mul_f32 v[12:13], v[10:11], v[12:13] op_sel_hi:[0,1]
	v_med3_f32 v11, v5, s79, v189
	v_cvt_pk_fp8_f32 v4, v3, v6
	v_med3_f32 v3, v14, s79, v189
	v_med3_f32 v6, v15, s79, v189
	v_mov_b32_e32 v5, v179
	v_cvt_pk_fp8_f32 v5, v3, v6
	v_med3_f32 v3, v12, s79, v189
	v_med3_f32 v6, v13, s79, v189
	v_cvt_pk_fp8_f32 v4, v7, v11 op_sel:[0,0,1]
	v_cvt_pk_fp8_f32 v5, v3, v6 op_sel:[0,0,1]
	v_mul_f32_e32 v12, 0x42000000, v196
	v_pk_fma_f32 v[6:7], v[168:169], s[10:11], v[48:49] op_sel_hi:[1,0,1]
	v_pk_fma_f32 v[14:15], v[166:167], s[10:11], v[46:47] op_sel_hi:[1,0,1]
	v_pk_mul_f32 v[6:7], v[12:13], v[6:7] op_sel_hi:[0,1]
	v_pk_mul_f32 v[14:15], v[12:13], v[14:15] op_sel_hi:[0,1]
	v_pk_fma_f32 v[16:17], v[164:165], s[10:11], v[44:45] op_sel_hi:[1,0,1]
	v_pk_fma_f32 v[18:19], v[162:163], s[10:11], v[42:43] op_sel_hi:[1,0,1]
	v_pk_mul_f32 v[16:17], v[12:13], v[16:17] op_sel_hi:[0,1]
	v_pk_mul_f32 v[18:19], v[12:13], v[18:19] op_sel_hi:[0,1]
	v_med3_f32 v3, v14, s79, v189
	v_med3_f32 v11, v15, s79, v189
	v_med3_f32 v13, v6, s79, v189
	v_mov_b32_e32 v6, v179
	v_med3_f32 v14, v7, s79, v189
	v_cvt_pk_fp8_f32 v6, v3, v11
	v_med3_f32 v3, v18, s79, v189
	v_med3_f32 v11, v19, s79, v189
	v_mov_b32_e32 v7, v179
	v_cvt_pk_fp8_f32 v7, v3, v11
	v_med3_f32 v3, v16, s79, v189
	v_med3_f32 v11, v17, s79, v189
	v_cvt_pk_fp8_f32 v6, v13, v14 op_sel:[0,0,1]
	v_cvt_pk_fp8_f32 v7, v3, v11 op_sel:[0,0,1]
	s_ashr_i32 s25, s24, 31
	v_lshl_add_u64 v[8:9], s[6:7], 0, v[8:9]
	v_lshl_add_u64 v[8:9], v[8:9], 0, s[24:25]
	v_permlane16_swap_b32_e32 v4, v6
	v_permlane16_swap_b32_e32 v5, v7
	v_lshl_add_u64 v[8:9], v[8:9], 0, v[178:179]
	global_store_dwordx4 v[8:9], v[4:7], off
	v_pk_fma_f32 v[14:15], v[156:157], s[10:11], v[36:37] op_sel_hi:[1,0,1]
	v_pk_fma_f32 v[16:17], v[154:155], s[10:11], v[34:35] op_sel_hi:[1,0,1]
	v_pk_fma_f32 v[4:5], v[160:161], s[10:11], v[40:41] op_sel_hi:[1,0,1]
	v_pk_fma_f32 v[6:7], v[158:159], s[10:11], v[38:39] op_sel_hi:[1,0,1]
	v_pk_mul_f32 v[4:5], v[10:11], v[4:5] op_sel_hi:[0,1]
	v_pk_mul_f32 v[6:7], v[10:11], v[6:7] op_sel_hi:[0,1]
	v_pk_mul_f32 v[14:15], v[10:11], v[14:15] op_sel_hi:[0,1]
	v_pk_mul_f32 v[10:11], v[10:11], v[16:17] op_sel_hi:[0,1]
	v_med3_f32 v3, v6, s79, v189
	v_med3_f32 v6, v7, s79, v189
	v_med3_f32 v7, v4, s79, v189
	v_mov_b32_e32 v4, v179
	v_med3_f32 v13, v5, s79, v189
	v_cvt_pk_fp8_f32 v4, v3, v6
	v_med3_f32 v3, v10, s79, v189
	v_med3_f32 v6, v11, s79, v189
	v_mov_b32_e32 v5, v179
	v_cvt_pk_fp8_f32 v5, v3, v6
	v_med3_f32 v3, v14, s79, v189
	v_med3_f32 v6, v15, s79, v189
	v_cvt_pk_fp8_f32 v4, v7, v13 op_sel:[0,0,1]
	v_cvt_pk_fp8_f32 v5, v3, v6 op_sel:[0,0,1]
	v_pk_fma_f32 v[6:7], v[152:153], s[10:11], v[40:41] op_sel_hi:[1,0,1]
	v_pk_fma_f32 v[10:11], v[150:151], s[10:11], v[38:39] op_sel_hi:[1,0,1]
	v_pk_mul_f32 v[6:7], v[12:13], v[6:7] op_sel_hi:[0,1]
	v_pk_mul_f32 v[10:11], v[12:13], v[10:11] op_sel_hi:[0,1]
	v_pk_fma_f32 v[14:15], v[148:149], s[10:11], v[36:37] op_sel_hi:[1,0,1]
	v_pk_fma_f32 v[16:17], v[146:147], s[10:11], v[34:35] op_sel_hi:[1,0,1]
	v_pk_mul_f32 v[14:15], v[12:13], v[14:15] op_sel_hi:[0,1]
	v_pk_mul_f32 v[12:13], v[12:13], v[16:17] op_sel_hi:[0,1]
	v_med3_f32 v3, v10, s79, v189
	v_med3_f32 v10, v11, s79, v189
	v_med3_f32 v11, v6, s79, v189
	v_mov_b32_e32 v6, v179
	v_med3_f32 v16, v7, s79, v189
	v_cvt_pk_fp8_f32 v6, v3, v10
	v_med3_f32 v3, v12, s79, v189
	v_med3_f32 v10, v13, s79, v189
	v_mov_b32_e32 v7, v179
	v_cvt_pk_fp8_f32 v7, v3, v10
	v_med3_f32 v3, v14, s79, v189
	v_med3_f32 v10, v15, s79, v189
	v_cvt_pk_fp8_f32 v6, v11, v16 op_sel:[0,0,1]
	v_cvt_pk_fp8_f32 v7, v3, v10 op_sel:[0,0,1]
	v_mul_f32_e32 v10, 0x42000000, v195
	v_pk_fma_f32 v[14:15], v[138:139], s[10:11], v[42:43] op_sel_hi:[1,0,1]
	v_permlane16_swap_b32_e32 v4, v6
	v_permlane16_swap_b32_e32 v5, v7
	global_store_dwordx4 v[8:9], v[4:7], off offset:128
	v_pk_fma_f32 v[12:13], v[140:141], s[10:11], v[44:45] op_sel_hi:[1,0,1]
	v_pk_mul_f32 v[14:15], v[10:11], v[14:15] op_sel_hi:[0,1]
	v_or_b32_e32 v4, 32, v2
	v_ashrrev_i32_e32 v5, 31, v4
	v_lshlrev_b64 v[8:9], 11, v[4:5]
	v_pk_fma_f32 v[4:5], v[144:145], s[10:11], v[48:49] op_sel_hi:[1,0,1]
	v_pk_fma_f32 v[6:7], v[142:143], s[10:11], v[46:47] op_sel_hi:[1,0,1]
	v_pk_mul_f32 v[4:5], v[10:11], v[4:5] op_sel_hi:[0,1]
	v_pk_mul_f32 v[6:7], v[10:11], v[6:7] op_sel_hi:[0,1]
	v_med3_f32 v3, v6, s79, v189
	v_med3_f32 v6, v7, s79, v189
	v_med3_f32 v7, v4, s79, v189
	v_mov_b32_e32 v4, v179
	v_pk_mul_f32 v[12:13], v[10:11], v[12:13] op_sel_hi:[0,1]
	v_med3_f32 v11, v5, s79, v189
	v_cvt_pk_fp8_f32 v4, v3, v6
	v_med3_f32 v3, v14, s79, v189
	v_med3_f32 v6, v15, s79, v189
	v_mov_b32_e32 v5, v179
; __device__ __forceinline__ float sat8(float x) { return __builtin_amdgcn_fmed3f(x, -448.0f, 448.0f); }
; __device__ __forceinline__ unsigned pk4_fp8(float a, float b, float c, float d) { int v = 0; v = __builtin_amdgcn_cvt_pk_fp8_f32(a, b, v, false); v = __builtin_amdgcn_cvt_pk_fp8_f32(c, d, v, true); return (unsigned)v; }
;     __device__ __forceinline__ void operator()(const f32x4 (&acc)[2][2][4][2], const pg8::Unit& u, const Pre& q, int wr, int wc, int fr, int fq) const {
;         const int rl0 = wr * 64 + fr, colw = u.pn * 256 + wc * 32;
;         constexpr float DS = 1.0f / (FP8_SH * FP8_SW);
; #pragma unroll
;         for (int ai = 0; ai < 2; ++ai)
; #pragma unroll
;             for (int mp = 0; mp < 2; ++mp)
; #pragma unroll
;                 for (int bj = 0; bj < 2; ++bj) { unsigned lo[2], hi[2];
; #pragma unroll
;                     for (int mm = 0; mm < 2; ++mm) { const int m = 2 * mp + mm; const float gt = q.gt[ai][m] * FP8_SY;
;                         const f32x4 v0 = (acc[ai][bj][m][0] * DS + q.bv[bj][0]) * gt, v1 = (acc[ai][bj][m][1] * DS + q.bv[bj][1]) * gt;
;                         lo[mm] = pk4_fp8(sat8(v0[0]), sat8(v0[1]), sat8(v0[2]), sat8(v0[3])); hi[mm] = pk4_fp8(sat8(v1[0]), sat8(v1[1]), sat8(v1[2]), sat8(v1[3])); }
;                     const v2u r0 = __builtin_amdgcn_permlane16_swap(lo[0], lo[1], false, false), r1 = __builtin_amdgcn_permlane16_swap(hi[0], hi[1], false, false);
;                     unsigned char* rowp = y2 + (size_t)(u.pm * 256 + rl0 + ai * 128 + (2 * mp + (fq & 1)) * 16) * D + colw + bj * 128 + 16 * (fq >> 1);
;                     *(v4u*)rowp = (v4u){r0.x, r1.x, r0.y, r1.y}; }
	v_cvt_pk_fp8_f32 v5, v3, v6
	v_med3_f32 v3, v12, s79, v189
	v_med3_f32 v6, v13, s79, v189
	v_cvt_pk_fp8_f32 v4, v7, v11 op_sel:[0,0,1]
	v_cvt_pk_fp8_f32 v5, v3, v6 op_sel:[0,0,1]
	v_mul_f32_e32 v12, 0x42000000, v194
	v_pk_fma_f32 v[6:7], v[136:137], s[10:11], v[48:49] op_sel_hi:[1,0,1]
	v_pk_fma_f32 v[14:15], v[134:135], s[10:11], v[46:47] op_sel_hi:[1,0,1]
	v_pk_mul_f32 v[6:7], v[12:13], v[6:7] op_sel_hi:[0,1]
	v_pk_mul_f32 v[14:15], v[12:13], v[14:15] op_sel_hi:[0,1]
	v_pk_fma_f32 v[16:17], v[132:133], s[10:11], v[44:45] op_sel_hi:[1,0,1]
	v_pk_fma_f32 v[18:19], v[130:131], s[10:11], v[42:43] op_sel_hi:[1,0,1]
	v_pk_mul_f32 v[16:17], v[12:13], v[16:17] op_sel_hi:[0,1]
	v_pk_mul_f32 v[18:19], v[12:13], v[18:19] op_sel_hi:[0,1]
	v_med3_f32 v3, v14, s79, v189
	v_med3_f32 v11, v15, s79, v189
	v_med3_f32 v13, v6, s79, v189
	v_mov_b32_e32 v6, v179
	v_med3_f32 v14, v7, s79, v189
	v_cvt_pk_fp8_f32 v6, v3, v11
	v_med3_f32 v3, v18, s79, v189
	v_med3_f32 v11, v19, s79, v189
	v_mov_b32_e32 v7, v179
	v_cvt_pk_fp8_f32 v7, v3, v11
	v_med3_f32 v3, v16, s79, v189
	v_med3_f32 v11, v17, s79, v189
	v_cvt_pk_fp8_f32 v6, v13, v14 op_sel:[0,0,1]
	v_cvt_pk_fp8_f32 v7, v3, v11 op_sel:[0,0,1]
	v_lshl_add_u64 v[8:9], s[6:7], 0, v[8:9]
	v_lshl_add_u64 v[8:9], v[8:9], 0, s[24:25]
	v_permlane16_swap_b32_e32 v4, v6
	v_permlane16_swap_b32_e32 v5, v7
	v_lshl_add_u64 v[8:9], v[8:9], 0, v[178:179]
	global_store_dwordx4 v[8:9], v[4:7], off
	v_pk_fma_f32 v[14:15], v[124:125], s[10:11], v[36:37] op_sel_hi:[1,0,1]
	v_pk_fma_f32 v[16:17], v[122:123], s[10:11], v[34:35] op_sel_hi:[1,0,1]
	v_pk_fma_f32 v[4:5], v[128:129], s[10:11], v[40:41] op_sel_hi:[1,0,1]
	v_pk_fma_f32 v[6:7], v[126:127], s[10:11], v[38:39] op_sel_hi:[1,0,1]
	v_pk_mul_f32 v[4:5], v[10:11], v[4:5] op_sel_hi:[0,1]
	v_pk_mul_f32 v[6:7], v[10:11], v[6:7] op_sel_hi:[0,1]
	v_pk_mul_f32 v[14:15], v[10:11], v[14:15] op_sel_hi:[0,1]
	v_pk_mul_f32 v[10:11], v[10:11], v[16:17] op_sel_hi:[0,1]
	v_med3_f32 v3, v6, s79, v189
	v_med3_f32 v6, v7, s79, v189
	v_med3_f32 v7, v4, s79, v189
	v_mov_b32_e32 v4, v179
	v_med3_f32 v13, v5, s79, v189
	v_cvt_pk_fp8_f32 v4, v3, v6
	v_med3_f32 v3, v10, s79, v189
	v_med3_f32 v6, v11, s79, v189
	v_mov_b32_e32 v5, v179
	v_cvt_pk_fp8_f32 v5, v3, v6
	v_med3_f32 v3, v14, s79, v189
	v_med3_f32 v6, v15, s79, v189
	v_cvt_pk_fp8_f32 v4, v7, v13 op_sel:[0,0,1]
	v_cvt_pk_fp8_f32 v5, v3, v6 op_sel:[0,0,1]
	v_pk_fma_f32 v[6:7], v[120:121], s[10:11], v[40:41] op_sel_hi:[1,0,1]
	v_pk_fma_f32 v[10:11], v[118:119], s[10:11], v[38:39] op_sel_hi:[1,0,1]
	v_pk_mul_f32 v[6:7], v[12:13], v[6:7] op_sel_hi:[0,1]
	v_pk_mul_f32 v[10:11], v[12:13], v[10:11] op_sel_hi:[0,1]
	v_pk_fma_f32 v[14:15], v[116:117], s[10:11], v[36:37] op_sel_hi:[1,0,1]
	v_pk_fma_f32 v[16:17], v[114:115], s[10:11], v[34:35] op_sel_hi:[1,0,1]
	v_pk_mul_f32 v[14:15], v[12:13], v[14:15] op_sel_hi:[0,1]
	v_pk_mul_f32 v[12:13], v[12:13], v[16:17] op_sel_hi:[0,1]
	v_med3_f32 v3, v10, s79, v189
	v_med3_f32 v10, v11, s79, v189
	v_med3_f32 v11, v6, s79, v189
	v_mov_b32_e32 v6, v179
	v_med3_f32 v16, v7, s79, v189
	v_cvt_pk_fp8_f32 v6, v3, v10
	v_med3_f32 v3, v12, s79, v189
	v_med3_f32 v10, v13, s79, v189
	v_mov_b32_e32 v7, v179
	v_cvt_pk_fp8_f32 v7, v3, v10
	v_med3_f32 v3, v14, s79, v189
	v_med3_f32 v10, v15, s79, v189
	v_cvt_pk_fp8_f32 v6, v11, v16 op_sel:[0,0,1]
	v_cvt_pk_fp8_f32 v7, v3, v10 op_sel:[0,0,1]
	v_mul_f32_e32 v10, 0x42000000, v193
	v_pk_fma_f32 v[14:15], v[106:107], s[10:11], v[42:43] op_sel_hi:[1,0,1]
	v_permlane16_swap_b32_e32 v4, v6
	v_permlane16_swap_b32_e32 v5, v7
	global_store_dwordx4 v[8:9], v[4:7], off offset:128
	v_pk_fma_f32 v[12:13], v[108:109], s[10:11], v[44:45] op_sel_hi:[1,0,1]
	v_pk_mul_f32 v[14:15], v[10:11], v[14:15] op_sel_hi:[0,1]
	v_add_u32_e32 v4, 0x80, v2
	v_ashrrev_i32_e32 v5, 31, v4
	v_lshlrev_b64 v[8:9], 11, v[4:5]
	v_pk_fma_f32 v[4:5], v[112:113], s[10:11], v[48:49] op_sel_hi:[1,0,1]
	v_pk_fma_f32 v[6:7], v[110:111], s[10:11], v[46:47] op_sel_hi:[1,0,1]
	v_pk_mul_f32 v[4:5], v[10:11], v[4:5] op_sel_hi:[0,1]
	v_pk_mul_f32 v[6:7], v[10:11], v[6:7] op_sel_hi:[0,1]
	v_med3_f32 v3, v6, s79, v189
	v_med3_f32 v6, v7, s79, v189
	v_med3_f32 v7, v4, s79, v189
	v_mov_b32_e32 v4, v179
	v_pk_mul_f32 v[12:13], v[10:11], v[12:13] op_sel_hi:[0,1]
	v_med3_f32 v11, v5, s79, v189
	v_cvt_pk_fp8_f32 v4, v3, v6
	v_med3_f32 v3, v14, s79, v189
	v_med3_f32 v6, v15, s79, v189
	v_mov_b32_e32 v5, v179
	v_cvt_pk_fp8_f32 v5, v3, v6
	v_med3_f32 v3, v12, s79, v189
	v_med3_f32 v6, v13, s79, v189
	v_cvt_pk_fp8_f32 v4, v7, v11 op_sel:[0,0,1]
	v_cvt_pk_fp8_f32 v5, v3, v6 op_sel:[0,0,1]
	v_mul_f32_e32 v12, 0x42000000, v192
	v_pk_fma_f32 v[6:7], v[104:105], s[10:11], v[48:49] op_sel_hi:[1,0,1]
	v_pk_fma_f32 v[14:15], v[102:103], s[10:11], v[46:47] op_sel_hi:[1,0,1]
	v_pk_mul_f32 v[6:7], v[12:13], v[6:7] op_sel_hi:[0,1]
	v_pk_mul_f32 v[14:15], v[12:13], v[14:15] op_sel_hi:[0,1]
	v_pk_fma_f32 v[16:17], v[100:101], s[10:11], v[44:45] op_sel_hi:[1,0,1]
	v_pk_fma_f32 v[18:19], v[98:99], s[10:11], v[42:43] op_sel_hi:[1,0,1]
	v_pk_mul_f32 v[16:17], v[12:13], v[16:17] op_sel_hi:[0,1]
	v_pk_mul_f32 v[18:19], v[12:13], v[18:19] op_sel_hi:[0,1]
	v_med3_f32 v3, v14, s79, v189
	v_med3_f32 v11, v15, s79, v189
	v_med3_f32 v13, v6, s79, v189
	v_mov_b32_e32 v6, v179
	v_med3_f32 v14, v7, s79, v189
	v_cvt_pk_fp8_f32 v6, v3, v11
	v_med3_f32 v3, v18, s79, v189
	v_med3_f32 v11, v19, s79, v189
	v_mov_b32_e32 v7, v179
	v_cvt_pk_fp8_f32 v7, v3, v11
	v_med3_f32 v3, v16, s79, v189
	v_med3_f32 v11, v17, s79, v189
	v_cvt_pk_fp8_f32 v6, v13, v14 op_sel:[0,0,1]
	v_cvt_pk_fp8_f32 v7, v3, v11 op_sel:[0,0,1]
	v_lshl_add_u64 v[8:9], s[6:7], 0, v[8:9]
	v_lshl_add_u64 v[8:9], v[8:9], 0, s[24:25]
; __device__ __forceinline__ float sat8(float x) { return __builtin_amdgcn_fmed3f(x, -448.0f, 448.0f); }
; __device__ __forceinline__ unsigned pk4_fp8(float a, float b, float c, float d) { int v = 0; v = __builtin_amdgcn_cvt_pk_fp8_f32(a, b, v, false); v = __builtin_amdgcn_cvt_pk_fp8_f32(c, d, v, true); return (unsigned)v; }
;     __device__ __forceinline__ void operator()(const f32x4 (&acc)[2][2][4][2], const pg8::Unit& u, const Pre& q, int wr, int wc, int fr, int fq) const {
;         const int rl0 = wr * 64 + fr, colw = u.pn * 256 + wc * 32;
;         constexpr float DS = 1.0f / (FP8_SH * FP8_SW);
; #pragma unroll
;         for (int ai = 0; ai < 2; ++ai)
; #pragma unroll
;             for (int mp = 0; mp < 2; ++mp)
; #pragma unroll
;                 for (int bj = 0; bj < 2; ++bj) { unsigned lo[2], hi[2];
; #pragma unroll
;                     for (int mm = 0; mm < 2; ++mm) { const int m = 2 * mp + mm; const float gt = q.gt[ai][m] * FP8_SY;
;                         const f32x4 v0 = (acc[ai][bj][m][0] * DS + q.bv[bj][0]) * gt, v1 = (acc[ai][bj][m][1] * DS + q.bv[bj][1]) * gt;
;                         lo[mm] = pk4_fp8(sat8(v0[0]), sat8(v0[1]), sat8(v0[2]), sat8(v0[3])); hi[mm] = pk4_fp8(sat8(v1[0]), sat8(v1[1]), sat8(v1[2]), sat8(v1[3])); }
;                     const v2u r0 = __builtin_amdgcn_permlane16_swap(lo[0], lo[1], false, false), r1 = __builtin_amdgcn_permlane16_swap(hi[0], hi[1], false, false);
;                     unsigned char* rowp = y2 + (size_t)(u.pm * 256 + rl0 + ai * 128 + (2 * mp + (fq & 1)) * 16) * D + colw + bj * 128 + 16 * (fq >> 1);
;                     *(v4u*)rowp = (v4u){r0.x, r1.x, r0.y, r1.y}; }
	v_permlane16_swap_b32_e32 v4, v6
	v_permlane16_swap_b32_e32 v5, v7
	v_lshl_add_u64 v[8:9], v[8:9], 0, v[178:179]
	global_store_dwordx4 v[8:9], v[4:7], off
	v_pk_fma_f32 v[14:15], v[92:93], s[10:11], v[36:37] op_sel_hi:[1,0,1]
	v_pk_fma_f32 v[16:17], v[90:91], s[10:11], v[34:35] op_sel_hi:[1,0,1]
	v_pk_fma_f32 v[4:5], v[96:97], s[10:11], v[40:41] op_sel_hi:[1,0,1]
	v_pk_fma_f32 v[6:7], v[94:95], s[10:11], v[38:39] op_sel_hi:[1,0,1]
	v_pk_mul_f32 v[4:5], v[10:11], v[4:5] op_sel_hi:[0,1]
	v_pk_mul_f32 v[6:7], v[10:11], v[6:7] op_sel_hi:[0,1]
	v_pk_mul_f32 v[14:15], v[10:11], v[14:15] op_sel_hi:[0,1]
	v_pk_mul_f32 v[10:11], v[10:11], v[16:17] op_sel_hi:[0,1]
	v_med3_f32 v3, v6, s79, v189
	v_med3_f32 v6, v7, s79, v189
	v_med3_f32 v7, v4, s79, v189
	v_mov_b32_e32 v4, v179
	v_med3_f32 v13, v5, s79, v189
	v_cvt_pk_fp8_f32 v4, v3, v6
	v_med3_f32 v3, v10, s79, v189
	v_med3_f32 v6, v11, s79, v189
	v_mov_b32_e32 v5, v179
	v_cvt_pk_fp8_f32 v5, v3, v6
	v_med3_f32 v3, v14, s79, v189
	v_med3_f32 v6, v15, s79, v189
	v_cvt_pk_fp8_f32 v4, v7, v13 op_sel:[0,0,1]
	v_cvt_pk_fp8_f32 v5, v3, v6 op_sel:[0,0,1]
	v_pk_fma_f32 v[6:7], v[88:89], s[10:11], v[40:41] op_sel_hi:[1,0,1]
	v_pk_fma_f32 v[10:11], v[86:87], s[10:11], v[38:39] op_sel_hi:[1,0,1]
	v_pk_mul_f32 v[6:7], v[12:13], v[6:7] op_sel_hi:[0,1]
	v_pk_mul_f32 v[10:11], v[12:13], v[10:11] op_sel_hi:[0,1]
	v_pk_fma_f32 v[14:15], v[84:85], s[10:11], v[36:37] op_sel_hi:[1,0,1]
	v_pk_fma_f32 v[16:17], v[82:83], s[10:11], v[34:35] op_sel_hi:[1,0,1]
	v_pk_mul_f32 v[14:15], v[12:13], v[14:15] op_sel_hi:[0,1]
	v_pk_mul_f32 v[12:13], v[12:13], v[16:17] op_sel_hi:[0,1]
	v_med3_f32 v3, v10, s79, v189
	v_med3_f32 v10, v11, s79, v189
	v_med3_f32 v11, v6, s79, v189
	v_mov_b32_e32 v6, v179
	v_med3_f32 v16, v7, s79, v189
	v_cvt_pk_fp8_f32 v6, v3, v10
	v_med3_f32 v3, v12, s79, v189
	v_med3_f32 v10, v13, s79, v189
	v_mov_b32_e32 v7, v179
	v_cvt_pk_fp8_f32 v7, v3, v10
	v_med3_f32 v3, v14, s79, v189
	v_med3_f32 v10, v15, s79, v189
	v_cvt_pk_fp8_f32 v6, v11, v16 op_sel:[0,0,1]
	v_cvt_pk_fp8_f32 v7, v3, v10 op_sel:[0,0,1]
	v_add_u32_e32 v2, 0xa0, v2
	v_ashrrev_i32_e32 v3, 31, v2
	v_permlane16_swap_b32_e32 v4, v6
	v_permlane16_swap_b32_e32 v5, v7
	global_store_dwordx4 v[8:9], v[4:7], off offset:128
	v_mul_f32_e32 v8, 0x42000000, v191
	v_pk_fma_f32 v[10:11], v[76:77], s[10:11], v[44:45] op_sel_hi:[1,0,1]
	v_lshlrev_b64 v[6:7], 11, v[2:3]
	v_pk_fma_f32 v[2:3], v[80:81], s[10:11], v[48:49] op_sel_hi:[1,0,1]
	v_pk_fma_f32 v[4:5], v[78:79], s[10:11], v[46:47] op_sel_hi:[1,0,1]
	v_pk_mul_f32 v[2:3], v[8:9], v[2:3] op_sel_hi:[0,1]
	v_pk_mul_f32 v[4:5], v[8:9], v[4:5] op_sel_hi:[0,1]
	v_pk_fma_f32 v[12:13], v[74:75], s[10:11], v[42:43] op_sel_hi:[1,0,1]
	v_pk_mul_f32 v[10:11], v[8:9], v[10:11] op_sel_hi:[0,1]
	v_pk_mul_f32 v[12:13], v[8:9], v[12:13] op_sel_hi:[0,1]
	v_med3_f32 v4, v4, s79, v189
	v_med3_f32 v5, v5, s79, v189
	v_med3_f32 v9, v2, s79, v189
	v_mov_b32_e32 v2, v179
	v_med3_f32 v14, v3, s79, v189
	v_cvt_pk_fp8_f32 v2, v4, v5
	v_med3_f32 v4, v12, s79, v189
	v_med3_f32 v5, v13, s79, v189
	v_mov_b32_e32 v3, v179
	v_cvt_pk_fp8_f32 v3, v4, v5
	v_med3_f32 v4, v10, s79, v189
	v_med3_f32 v5, v11, s79, v189
	v_mul_f32_e32 v10, 0x42000000, v190
	v_cvt_pk_fp8_f32 v3, v4, v5 op_sel:[0,0,1]
	v_pk_fma_f32 v[4:5], v[72:73], s[10:11], v[48:49] op_sel_hi:[1,0,1]
	v_pk_fma_f32 v[12:13], v[70:71], s[10:11], v[46:47] op_sel_hi:[1,0,1]
	v_cvt_pk_fp8_f32 v2, v9, v14 op_sel:[0,0,1]
	v_pk_mul_f32 v[4:5], v[10:11], v[4:5] op_sel_hi:[0,1]
	v_pk_mul_f32 v[12:13], v[10:11], v[12:13] op_sel_hi:[0,1]
	v_pk_fma_f32 v[14:15], v[68:69], s[10:11], v[44:45] op_sel_hi:[1,0,1]
	v_pk_fma_f32 v[16:17], v[66:67], s[10:11], v[42:43] op_sel_hi:[1,0,1]
	v_pk_mul_f32 v[14:15], v[10:11], v[14:15] op_sel_hi:[0,1]
	v_pk_mul_f32 v[16:17], v[10:11], v[16:17] op_sel_hi:[0,1]
	v_med3_f32 v9, v12, s79, v189
	v_med3_f32 v11, v13, s79, v189
	v_med3_f32 v12, v4, s79, v189
	v_mov_b32_e32 v4, v179
	v_med3_f32 v13, v5, s79, v189
	v_cvt_pk_fp8_f32 v4, v9, v11
	v_med3_f32 v9, v16, s79, v189
	v_med3_f32 v11, v17, s79, v189
	v_mov_b32_e32 v5, v179
	v_cvt_pk_fp8_f32 v5, v9, v11
	v_med3_f32 v9, v14, s79, v189
	v_med3_f32 v11, v15, s79, v189
	v_cvt_pk_fp8_f32 v4, v12, v13 op_sel:[0,0,1]
	v_cvt_pk_fp8_f32 v5, v9, v11 op_sel:[0,0,1]
	v_lshl_add_u64 v[6:7], s[6:7], 0, v[6:7]
	v_lshl_add_u64 v[6:7], v[6:7], 0, s[24:25]
	v_permlane16_swap_b32_e32 v2, v4
	v_permlane16_swap_b32_e32 v3, v5
	v_lshl_add_u64 v[6:7], v[6:7], 0, v[178:179]
	global_store_dwordx4 v[6:7], v[2:5], off
	v_pk_fma_f32 v[12:13], v[60:61], s[10:11], v[36:37] op_sel_hi:[1,0,1]
	v_pk_fma_f32 v[14:15], v[58:59], s[10:11], v[34:35] op_sel_hi:[1,0,1]
	v_pk_fma_f32 v[2:3], v[64:65], s[10:11], v[40:41] op_sel_hi:[1,0,1]
	v_pk_fma_f32 v[4:5], v[62:63], s[10:11], v[38:39] op_sel_hi:[1,0,1]
	v_pk_mul_f32 v[2:3], v[8:9], v[2:3] op_sel_hi:[0,1]
	v_pk_mul_f32 v[4:5], v[8:9], v[4:5] op_sel_hi:[0,1]
	v_pk_mul_f32 v[12:13], v[8:9], v[12:13] op_sel_hi:[0,1]
	v_pk_mul_f32 v[8:9], v[8:9], v[14:15] op_sel_hi:[0,1]
	v_med3_f32 v4, v4, s79, v189
	v_med3_f32 v5, v5, s79, v189
	v_med3_f32 v11, v2, s79, v189
	v_mov_b32_e32 v2, v179
	v_med3_f32 v14, v3, s79, v189
	v_cvt_pk_fp8_f32 v2, v4, v5
	v_med3_f32 v4, v8, s79, v189
	v_med3_f32 v5, v9, s79, v189
	v_mov_b32_e32 v3, v179
	v_cvt_pk_fp8_f32 v3, v4, v5
	v_med3_f32 v4, v12, s79, v189
	v_med3_f32 v5, v13, s79, v189
	v_pk_fma_f32 v[8:9], v[54:55], s[10:11], v[38:39] op_sel_hi:[1,0,1]
	v_cvt_pk_fp8_f32 v3, v4, v5 op_sel:[0,0,1]
	v_pk_fma_f32 v[4:5], v[56:57], s[10:11], v[40:41] op_sel_hi:[1,0,1]
	v_cvt_pk_fp8_f32 v2, v11, v14 op_sel:[0,0,1]
	v_pk_mul_f32 v[4:5], v[10:11], v[4:5] op_sel_hi:[0,1]
	v_pk_mul_f32 v[8:9], v[10:11], v[8:9] op_sel_hi:[0,1]
	v_pk_fma_f32 v[12:13], v[52:53], s[10:11], v[36:37] op_sel_hi:[1,0,1]
	v_pk_fma_f32 v[14:15], v[50:51], s[10:11], v[34:35] op_sel_hi:[1,0,1]
	v_pk_mul_f32 v[12:13], v[10:11], v[12:13] op_sel_hi:[0,1]
	v_pk_mul_f32 v[10:11], v[10:11], v[14:15] op_sel_hi:[0,1]
	v_med3_f32 v8, v8, s79, v189
	v_med3_f32 v9, v9, s79, v189
	v_med3_f32 v14, v4, s79, v189
	v_mov_b32_e32 v4, v179
	v_med3_f32 v15, v5, s79, v189
	v_cvt_pk_fp8_f32 v4, v8, v9
	v_med3_f32 v8, v10, s79, v189
	v_med3_f32 v9, v11, s79, v189
	v_mov_b32_e32 v5, v179
	v_cvt_pk_fp8_f32 v5, v8, v9
	v_med3_f32 v8, v12, s79, v189
	v_med3_f32 v9, v13, s79, v189
	v_cvt_pk_fp8_f32 v4, v14, v15 op_sel:[0,0,1]
	v_cvt_pk_fp8_f32 v5, v8, v9 op_sel:[0,0,1]
	s_andn2_b64 vcc, exec, s[0:1]
	s_mov_b64 s[0:1], -1
	v_permlane16_swap_b32_e32 v2, v4
	v_permlane16_swap_b32_e32 v3, v5
	v_readlane_b32 s38, v255, 28
	global_store_dwordx4 v[6:7], v[2:5], off offset:128
	s_cbranch_vccnz .LBB0_803
; #define PG8_BAR __builtin_amdgcn_s_barrier()
; template <class Epi, class Sched>
; __device__ __forceinline__ void gemm_phase(LAS unsigned char* lds, const Sched& S, const Epi& E) {
;     ...
;         cur = nxt; cA = nA; cB = nB; crot = nrot; ++ui;
;         E.prefetch(cur, epre);
;         if (wr == 1) PG8_BAR;
;     __device__ __forceinline__ void prefetch(const pg8::Unit& u, Pre& q) const {
;         int tz = threadIdx.x; asm volatile("" : "+v"(tz)); const int wid = tz >> 6, wr = wid >> 2, wc = wid & 3, fr = tz & 15, fq = (tz >> 4) & 3;
;         const int rl0 = wr * 64 + fr, col0 = u.pn * 256 + wc * 32 + 8 * fq;
;         const int mt = __builtin_amdgcn_readfirstlane(u.pm - tstart[u.e]);
;         const float* gp = sgate + (size_t)u.e * T + mt * 256;
; #pragma unroll
;         for (int bj = 0; bj < 2; ++bj)
; #pragma unroll
;             for (int n = 0; n < 2; ++n) q.bv[bj][n] = *(const f32x4*)(b_down + (size_t)u.e * D + col0 + bj * 128 + 4 * n);
; #pragma unroll
;         for (int ai = 0; ai < 2; ++ai)
; #pragma unroll
;             for (int m = 0; m < 4; ++m) q.gt[ai][m] = gp[rl0 + ai * 128 + m * 16];
;     }
	s_lshl_b32 s0, s96, 2
	s_add_i32 s0, s0, 0
	s_add_i32 s0, s0, 0x27d00
	v_mov_b32_e32 v4, v0
	v_mov_b32_e32 v2, s0
	ds_read_b32 v3, v2
	v_lshrrev_b32_e32 v2, 1, v4
	s_ashr_i32 s97, s96, 31
	v_readlane_b32 s16, v255, 29
	v_and_b32_e32 v2, 0x78, v2
	s_waitcnt lgkmcnt(0)
	v_sub_u32_e32 v3, s14, v3
	s_lshl_b64 s[0:1], s[96:97], 17
	v_readfirstlane_b32 s15, v3
	s_lshl_b32 s34, s15, 8
	s_ashr_i32 s35, s34, 31
	s_lshl_b64 s[36:37], s[96:97], 13
	v_readlane_b32 s26, v255, 39
	v_readlane_b32 s28, v255, 41
	v_lshl_or_b32 v2, s12, 8, v2
	v_readlane_b32 s27, v255, 40
	v_readlane_b32 s29, v255, 42
	s_add_u32 s26, s28, s36
	v_ashrrev_i32_e32 v3, 31, v2
	s_addc_u32 s27, s29, s37
	v_readlane_b32 s17, v255, 30
	v_lshl_add_u64 v[2:3], v[2:3], 2, s[26:27]
	s_add_u32 s15, s11, s0
	v_ashrrev_i32_e32 v5, 2, v4
	global_load_dwordx4 v[42:45], v[2:3], off offset:16
	global_load_dwordx4 v[46:49], v[2:3], off
	global_load_dwordx4 v[34:37], v[2:3], off offset:528
	global_load_dwordx4 v[38:41], v[2:3], off offset:512
	v_and_b32_e32 v2, 15, v4
	s_addc_u32 s17, s42, s1
	s_lshl_b64 s[0:1], s[34:35], 2
	v_and_or_b32 v2, v5, s91, v2
	s_add_u32 s0, s15, s0
	s_addc_u32 s1, s17, s1
	v_ashrrev_i32_e32 v3, 31, v2
	v_lshl_add_u64 v[2:3], v[2:3], 2, s[0:1]
	global_load_dword v197, v[2:3], off
	global_load_dword v196, v[2:3], off offset:64
	global_load_dword v195, v[2:3], off offset:128
	global_load_dword v194, v[2:3], off offset:192
	global_load_dword v193, v[2:3], off offset:512
	global_load_dword v192, v[2:3], off offset:576
	global_load_dword v191, v[2:3], off offset:640
	global_load_dword v190, v[2:3], off offset:704
	s_andn2_b64 vcc, exec, s[4:5]
	v_readlane_b32 s18, v255, 31
	v_readlane_b32 s19, v255, 32
	v_readlane_b32 s20, v255, 33
	v_readlane_b32 s21, v255, 34
	v_readlane_b32 s22, v255, 35
	v_readlane_b32 s23, v255, 36
	v_readlane_b32 s24, v255, 37
	v_readlane_b32 s25, v255, 38
	v_readlane_b32 s30, v255, 43
	v_readlane_b32 s31, v255, 44
	s_mov_b32 s100, 0
	s_cbranch_vccnz .LBB0_802
	s_mov_b32 s100, 1
	s_branch .LBB0_802
